# static priority raise for waves 4-7 added to the GQA attention units (now running without the rider)
# speedup vs baseline: 1.0098x; 1.0001x over previous
; DI f32x16 mfma8(v8i a, v8i b, f32x16 c) { return __builtin_amdgcn_mfma_scale_f32_32x32x64_f8f6f4(a, b, c, 0, 0, 0, 0, 0, 0); }
; DI void attn_unit_d8(unsigned char* lds, const AttnArgs& a) {
;     ...
;     auto tile = [&](const unsigned char* Kb, const unsigned char* Kn, v8i& Pa, v8i& Pb, v8i& v0, v8i& v1, const v8i& Qa, const v8i& Qb, const v8i& w0, const v8i& w1) __attribute__((always_inline)) {
;         qk(Kb, 1, s1a, s1b);
;         v0 = rd32(Kb + voff); v1 = rd32(Kb + voff + 32 * A8_PITCH);
;         o0[0] = mfma8(w0, Qa, o0[0]); o1[0] = mfma8(w0, Qb, o1[0]); o0[1] = mfma8(w1, Qa, o0[1]); o1[1] = mfma8(w1, Qb, o1[1]);
;         expsum(s0a, l0); expsum(s0b, l1); pack4(s0a, Pa, 0); pack4(s0b, Pb, 0);
;         qk(Kn, 0, s0a, s0b);
;         expsum(s1a, l0); expsum(s1b, l1); pack4(s1a, Pa, 4); pack4(s1b, Pb, 4);
; #pragma unroll
;         for (int i = 0; i < 8; ++i) { __builtin_amdgcn_sched_group_barrier(0x008, 1, 0); __builtin_amdgcn_sched_group_barrier(0x402, 22, 0); }
;     };
;     for (int t = a.t0; t < a.t1; t += 2) {
;         const int s1 = sb + 1 >= 5 ? sb - 4 : sb + 1, s2 = sb + 2 >= 5 ? sb - 3 : sb + 2, s3 = sb + 3 >= 5 ? sb - 2 : sb + 3, s4 = sb + 4 >= 5 ? sb - 1 : sb + 4;
;         { const int ta = t + 3, tb = t + 4; gload(ta < a.t1 ? ta : a.t1 - 1, kreg0, vreg0); gload(tb < a.t1 ? tb : a.t1 - 1, kreg1, vreg1); }
;         tile(lds + sb * D8_SLOT, lds + s1 * D8_SLOT, PaX, PbX, vX0, vX1, PaY, PbY, vY0, vY1);
;         tile(lds + s1 * D8_SLOT, lds + s2 * D8_SLOT, PaY, PbY, vY0, vY1, PaX, PbX, vX0, vX1);
;         lstore(s3, kreg0, vreg0); lstore(s4, kreg1, vreg1);
;         __syncthreads();
;         sb = s2;
;     }
.LBB0_663:
	s_cmp_gt_i32 s16, 3
	s_cselect_b32 s17, -4, 1
	s_add_i32 s18, s17, s16
	s_mul_i32 s6, s16, 0x2800
	s_cmp_gt_i32 s16, 2
	v_mfma_f32_32x32x64_f8f6f4 v[50:65], v[154:161], v[138:145], v[50:65]
	v_exp_f32_e32 v192, v90
	v_add_u32_e32 v90, s6, v218
	s_cselect_b32 s6, -3, 2
	s_add_i32 s6, s6, s16
	s_cmp_gt_i32 s16, 1
	s_cselect_b32 s19, -2, 3
	s_add_i32 s19, s19, s16
	s_cmp_gt_i32 s16, 0
	s_cselect_b32 s49, -1, 4
	s_min_u32 s54, s46, 64
	s_add_i32 s49, s49, s16
	s_cmp_lt_u32 s46, 61
	s_mul_i32 s17, s6, 0x2800
	s_mov_b32 s16, s6
	s_cselect_b64 s[52:53], -1, 0
	s_lshl_b32 s6, s54, 6
	s_add_i32 s54, s6, 0xc0
	s_add_i32 s55, s6, 0xfffff0c0
	s_and_b64 s[52:53], s[52:53], exec
	v_lshl_add_u64 v[98:99], v[182:183], 0, s[6:7]
	s_cselect_b32 s6, s54, s55
	s_cselect_b32 s53, s21, s48
	s_cselect_b32 s52, s20, s47
	s_min_u32 s56, s46, 63
	v_exp_f32_e32 v198, v82
	v_exp_f32_e32 v199, v83
	v_exp_f32_e32 v196, v84
	v_exp_f32_e32 v197, v85
	v_exp_f32_e32 v200, v86
	v_exp_f32_e32 v201, v87
	v_exp_f32_e32 v194, v88
	v_exp_f32_e32 v195, v89
	ds_read_b128 v[82:85], v90 offset:2560
	ds_read_b128 v[86:89], v90 offset:2576
	global_load_dwordx2 v[202:203], v[98:99], off offset:192
	v_add_u32_e32 v98, s6, v215
	s_cmp_lt_u32 s46, 60
	v_ashrrev_i32_e32 v99, 31, v98
	s_cselect_b64 s[54:55], -1, 0
	s_lshl_b32 s6, s56, 6
	v_lshlrev_b64 v[98:99], 8, v[98:99]
	s_add_i32 s56, s6, 0x100
	s_add_i32 s57, s6, 0xfffff100
	v_lshl_add_u64 v[98:99], s[52:53], 0, v[98:99]
	s_and_b64 s[52:53], s[54:55], exec
	s_cselect_b32 s54, s56, s57
	v_lshl_add_u64 v[220:221], v[98:99], 0, v[178:179]
	v_add_u32_e32 v98, s54, v215
	v_ashrrev_i32_e32 v99, 31, v98
	s_cselect_b32 s53, s21, s48
	s_cselect_b32 s52, s20, s47
	v_lshlrev_b64 v[98:99], 8, v[98:99]
	v_lshl_add_u64 v[100:101], v[182:183], 0, s[6:7]
	v_lshl_add_u64 v[98:99], s[52:53], 0, v[98:99]
	global_load_dwordx2 v[204:205], v[100:101], off offset:256
	v_lshl_add_u64 v[222:223], v[98:99], 0, v[178:179]
	s_waitcnt lgkmcnt(0)
	v_mfma_f32_32x32x64_f8f6f4 v[98:113], v[82:89], v[114:121], 0
	v_exp_f32_e32 v193, v91
	v_exp_f32_e32 v224, v92
	v_exp_f32_e32 v225, v93
	v_exp_f32_e32 v226, v94
	v_exp_f32_e32 v227, v95
	v_exp_f32_e32 v228, v96
	v_exp_f32_e32 v229, v97
	ds_read_b128 v[170:173], v90 offset:5120
	ds_read_b128 v[174:177], v90 offset:5136
	ds_read_b128 v[162:165], v90 offset:7680
	ds_read_b128 v[166:169], v90 offset:7696
	v_pk_add_f32 v[90:91], v[186:187], v[198:199]
	v_pk_add_f32 v[92:93], v[184:185], v[196:197]
	v_pk_add_f32 v[90:91], v[200:201], v[90:91]
	v_pk_add_f32 v[92:93], v[194:195], v[92:93]
	v_pk_add_f32 v[90:91], v[192:193], v[90:91]
	v_pk_add_f32 v[92:93], v[224:225], v[92:93]
	v_exp_f32_e32 v66, v66
	v_exp_f32_e32 v67, v67
	v_exp_f32_e32 v68, v68
	v_exp_f32_e32 v69, v69
	v_exp_f32_e32 v70, v70
	v_exp_f32_e32 v71, v71
	v_exp_f32_e32 v72, v72
	v_pk_add_f32 v[230:231], v[228:229], v[92:93]
	v_pk_add_f32 v[232:233], v[226:227], v[90:91]
	v_mfma_f32_32x32x64_f8f6f4 v[82:97], v[82:89], v[122:129], 0
	v_exp_f32_e32 v73, v73
	v_exp_f32_e32 v74, v74
	v_exp_f32_e32 v75, v75
	v_exp_f32_e32 v76, v76
	v_exp_f32_e32 v77, v77
	v_exp_f32_e32 v78, v78
	v_exp_f32_e32 v79, v79
	v_exp_f32_e32 v80, v80
	v_exp_f32_e32 v81, v81
	v_pk_add_f32 v[186:187], v[190:191], v[66:67]
	v_pk_add_f32 v[188:189], v[188:189], v[68:69]
	s_nop 0
	v_pk_add_f32 v[186:187], v[70:71], v[186:187]
	v_pk_add_f32 v[188:189], v[72:73], v[188:189]
	s_nop 0
	v_cvt_scalef32_pk_fp8_f32 v184, v198, v199, s36
	v_pk_add_f32 v[186:187], v[74:75], v[186:187]
	v_pk_add_f32 v[188:189], v[76:77], v[188:189]
	v_cvt_scalef32_pk_fp8_f32 v185, v200, v201, s36
	v_cvt_scalef32_pk_fp8_f32 v184, v196, v197, s36 op_sel:[0,0,0,1]
	v_pk_add_f32 v[190:191], v[78:79], v[186:187]
	v_pk_add_f32 v[188:189], v[80:81], v[188:189]
	v_mfma_f32_32x32x64_f8f6f4 v[2:17], v[154:161], v[130:137], v[2:17]
	s_nop 0
	s_nop 0
	s_nop 0
	s_nop 0
	s_nop 0
	s_nop 0
	s_mulk_i32 s18, 0x2800
	v_cvt_scalef32_pk_fp8_f32 v186, v192, v193, s36
	v_cvt_scalef32_pk_fp8_f32 v187, v226, v227, s36
	v_cvt_scalef32_pk_fp8_f32 v154, v66, v67, s36
	v_cvt_scalef32_pk_fp8_f32 v155, v70, v71, s36
	v_cvt_scalef32_pk_fp8_f32 v156, v74, v75, s36
	v_cvt_scalef32_pk_fp8_f32 v157, v78, v79, s36
	v_cvt_scalef32_pk_fp8_f32 v185, v194, v195, s36 op_sel:[0,0,0,1]
	v_add_u32_e32 v219, s18, v218
	v_cvt_scalef32_pk_fp8_f32 v186, v224, v225, s36 op_sel:[0,0,0,1]
	v_cvt_scalef32_pk_fp8_f32 v187, v228, v229, s36 op_sel:[0,0,0,1]
	v_cvt_scalef32_pk_fp8_f32 v154, v68, v69, s36 op_sel:[0,0,0,1]
	v_cvt_scalef32_pk_fp8_f32 v155, v72, v73, s36 op_sel:[0,0,0,1]
	v_cvt_scalef32_pk_fp8_f32 v156, v76, v77, s36 op_sel:[0,0,0,1]
	v_cvt_scalef32_pk_fp8_f32 v157, v80, v81, s36 op_sel:[0,0,0,1]
	v_exp_f32_e32 v98, v98
	v_exp_f32_e32 v99, v99
	v_mfma_f32_32x32x64_f8f6f4 v[34:49], v[146:153], v[138:145], v[34:49]
	v_exp_f32_e32 v100, v100
	v_exp_f32_e32 v101, v101
	v_exp_f32_e32 v102, v102
	v_exp_f32_e32 v103, v103
	v_exp_f32_e32 v104, v104
	v_exp_f32_e32 v105, v105
	v_exp_f32_e32 v106, v106
	v_exp_f32_e32 v107, v107
	v_exp_f32_e32 v108, v108
	v_exp_f32_e32 v109, v109
	v_exp_f32_e32 v110, v110
	v_exp_f32_e32 v111, v111
	v_exp_f32_e32 v112, v112
	v_exp_f32_e32 v113, v113
	ds_read_b128 v[192:195], v219
	ds_read_b128 v[196:199], v219 offset:16
	v_pk_add_f32 v[66:67], v[232:233], v[98:99]
	v_pk_add_f32 v[68:69], v[230:231], v[100:101]
	v_pk_add_f32 v[66:67], v[102:103], v[66:67]
	v_pk_add_f32 v[68:69], v[104:105], v[68:69]
	v_pk_add_f32 v[66:67], v[106:107], v[66:67]
	v_pk_add_f32 v[68:69], v[108:109], v[68:69]
	v_pk_add_f32 v[140:141], v[110:111], v[66:67]
	v_pk_add_f32 v[138:139], v[112:113], v[68:69]
	v_mfma_f32_32x32x64_f8f6f4 v[18:33], v[146:153], v[130:137], v[18:33]
	v_exp_f32_e32 v82, v82
	v_exp_f32_e32 v83, v83
	v_exp_f32_e32 v84, v84
	v_exp_f32_e32 v85, v85
	v_exp_f32_e32 v86, v86
	v_exp_f32_e32 v87, v87
	v_exp_f32_e32 v88, v88
	v_exp_f32_e32 v89, v89
	v_exp_f32_e32 v90, v90
	v_exp_f32_e32 v91, v91
	v_exp_f32_e32 v92, v92
	v_exp_f32_e32 v93, v93
	v_exp_f32_e32 v94, v94
	v_exp_f32_e32 v95, v95
	v_exp_f32_e32 v96, v96
	v_exp_f32_e32 v97, v97
	v_pk_add_f32 v[66:67], v[190:191], v[82:83]
	v_pk_add_f32 v[68:69], v[188:189], v[84:85]
	v_pk_add_f32 v[66:67], v[86:87], v[66:67]
	v_pk_add_f32 v[68:69], v[88:89], v[68:69]
	v_pk_add_f32 v[130:131], v[90:91], v[66:67]
	v_pk_add_f32 v[132:133], v[92:93], v[68:69]
	s_waitcnt lgkmcnt(0)
; DI KParamsPtr kparams() { KParamsPtr p = (KParamsPtr)__builtin_amdgcn_kernarg_segment_ptr(); asm volatile("" : "+s"(p)); return p; }
; DI void attn_unit_a8(unsigned char* lds, const AttnArgs& a) {
;     ...
;     auto w_decode = [&](int j, const float*& src, unsigned char*& dst, int& ld, int& n0, int& k0, bool& gu) __attribute__((always_inline)) {
;         const int g = (j >> 2) * 512 + a.wl, e = g / 96, rr = g - e * 96; KParamsPtr kp = kparams();
;         if (rr < 64) { src = kp->w_gu + ((size_t)a.wli * NE + e) * (1024 * 2048); dst = kp->ws + WS_WGU + (size_t)a.wli * SZ_WGU + (size_t)e * 2048 * 1024; ld = 2048; n0 = (rr & 7) * 256; k0 = ((rr >> 3) * 4 + (j & 3)) * 32; gu = true; }
;         else { const int q = rr - 64; src = kp->w_dn + ((size_t)a.wli * NE + e) * (1024 * 1024); dst = kp->ws + WS_WDN + (size_t)a.wli * SZ_WDN + (size_t)e * 1024 * 1024; ld = 1024; n0 = (q & 3) * 256; k0 = ((q >> 2) * 4 + (j & 3)) * 32; gu = false; } };
;     auto w_issue = [&](int j) __attribute__((always_inline)) { const float* src; unsigned char* dst; int ld, n0, k0; bool gu; w_decode(j, src, dst, ld, n0, k0, gu);
;         const float* p = src + (size_t)(k0 + 4 * wid) * ld + n0 + wn4;
;         wq[0] = __builtin_nontemporal_load((const f32x4*)p); wq[1] = __builtin_nontemporal_load((const f32x4*)(p + ld));
;         wq[2] = __builtin_nontemporal_load((const f32x4*)(p + (size_t)2 * ld)); wq[3] = __builtin_nontemporal_load((const f32x4*)(p + (size_t)3 * ld)); };
; DI void attn_unit_d8(unsigned char* lds, const AttnArgs& a) {
;     ...
;     auto tile = [&](const unsigned char* Kb, const unsigned char* Kn, v8i& Pa, v8i& Pb, v8i& v0, v8i& v1, const v8i& Qa, const v8i& Qb, const v8i& w0, const v8i& w1) __attribute__((always_inline)) {
;         qk(Kb, 1, s1a, s1b);
;         v0 = rd32(Kb + voff); v1 = rd32(Kb + voff + 32 * A8_PITCH);
;         o0[0] = mfma8(w0, Qa, o0[0]); o1[0] = mfma8(w0, Qb, o1[0]); o0[1] = mfma8(w1, Qa, o0[1]); o1[1] = mfma8(w1, Qb, o1[1]);
;         expsum(s0a, l0); expsum(s0b, l1); pack4(s0a, Pa, 0); pack4(s0b, Pb, 0);
;         qk(Kn, 0, s0a, s0b);
;         expsum(s1a, l0); expsum(s1b, l1); pack4(s1a, Pa, 4); pack4(s1b, Pb, 4);
; #pragma unroll
;         for (int i = 0; i < 8; ++i) { __builtin_amdgcn_sched_group_barrier(0x008, 1, 0); __builtin_amdgcn_sched_group_barrier(0x402, 22, 0); }
;     };
	v_mfma_f32_32x32x64_f8f6f4 v[66:81], v[192:199], v[114:121], 0
	s_nop 0
	s_nop 0
	s_nop 0
	s_nop 0
	s_nop 0
	s_nop 0
	s_nop 0
	v_cvt_scalef32_pk_fp8_f32 v188, v98, v99, s36
	v_cvt_scalef32_pk_fp8_f32 v189, v102, v103, s36
	v_cvt_scalef32_pk_fp8_f32 v190, v106, v107, s36
	v_cvt_scalef32_pk_fp8_f32 v191, v110, v111, s36
	v_cvt_scalef32_pk_fp8_f32 v158, v82, v83, s36
	v_cvt_scalef32_pk_fp8_f32 v159, v86, v87, s36
	v_pk_add_f32 v[142:143], v[96:97], v[132:133]
	v_pk_add_f32 v[144:145], v[94:95], v[130:131]
	v_cvt_scalef32_pk_fp8_f32 v160, v90, v91, s36
	v_cvt_scalef32_pk_fp8_f32 v188, v100, v101, s36 op_sel:[0,0,0,1]
	v_cvt_scalef32_pk_fp8_f32 v189, v104, v105, s36 op_sel:[0,0,0,1]
	v_cvt_scalef32_pk_fp8_f32 v190, v108, v109, s36 op_sel:[0,0,0,1]
	v_cvt_scalef32_pk_fp8_f32 v191, v112, v113, s36 op_sel:[0,0,0,1]
	v_cvt_scalef32_pk_fp8_f32 v158, v84, v85, s36 op_sel:[0,0,0,1]
	v_cvt_scalef32_pk_fp8_f32 v159, v88, v89, s36 op_sel:[0,0,0,1]
	v_mfma_f32_32x32x64_f8f6f4 v[98:113], v[192:199], v[122:129], 0
	global_load_dwordx2 v[192:193], v[220:221], off
	global_load_dwordx2 v[194:195], v[222:223], off
	ds_read_b128 v[130:133], v219 offset:2560
	ds_read_b128 v[134:137], v219 offset:2576
	s_mulk_i32 s19, 0x2800
	s_nop 0
	v_exp_f32_e32 v146, v66
	s_add_i32 s80, s61, 0
	v_exp_f32_e32 v147, v67
	s_lshr_b32 s73, s80, 2
	v_exp_f32_e32 v148, v68
	s_lshl_b32 s73, s73, 9
	v_exp_f32_e32 v149, v69
	s_add_i32 s73, s73, s42
	s_add_i32 s19, s19, 0
	v_cvt_scalef32_pk_fp8_f32 v161, v94, v95, s36
	v_exp_f32_e32 v150, v70
	s_mul_i32 s75, s73, 0xaaab
	v_exp_f32_e32 v151, v71
	s_lshr_b32 s75, s75, 22
	v_exp_f32_e32 v152, v72
	s_mul_i32 s76, s75, 0x60
	v_exp_f32_e32 v153, v73
	s_sub_i32 s76, s73, s76
	v_add_u32_e32 v224, s19, v216
	v_add_u32_e32 v225, s19, v217
	v_cvt_scalef32_pk_fp8_f32 v160, v92, v93, s36 op_sel:[0,0,0,1]
	v_cvt_scalef32_pk_fp8_f32 v161, v96, v97, s36 op_sel:[0,0,0,1]
	v_exp_f32_e32 v196, v74
	s_lshr_b32 s77, s76, 6
	v_exp_f32_e32 v197, v75
	s_lshl_b32 s78, s77, 6
	v_exp_f32_e32 v198, v76
	s_sub_i32 s76, s76, s78
	v_exp_f32_e32 v199, v77
	s_sub_i32 s78, 3, s77
	v_exp_f32_e32 v200, v78
	s_lshr_b32 s79, s76, s78
	v_exp_f32_e32 v201, v79
	s_lshl_b32 s79, s79, 2
	v_exp_f32_e32 v220, v80
	s_and_b32 s81, s80, 3
	v_exp_f32_e32 v221, v81
	s_add_i32 s79, s79, s81
	s_waitcnt lgkmcnt(0)
	v_mfma_f32_32x32x64_f8f6f4 v[82:97], v[130:137], v[114:121], 0
	v_add_f32_e64 v66, v140, v146
	v_add_f32_e64 v67, v141, v147
	v_add_f32_e64 v68, v138, v148
	v_add_f32_e64 v69, v139, v149
	v_add_f32_e64 v66, v150, v66
	v_add_f32_e64 v67, v151, v67
	v_add_f32_e64 v68, v152, v68
	v_add_f32_e64 v69, v153, v69
	v_add_f32_e64 v138, v196, v66
	v_add_f32_e64 v139, v197, v67
	v_add_f32_e64 v140, v198, v68
	v_add_f32_e64 v141, v199, v69
	v_exp_f32_e32 v98, v98
	s_lshl_b32 s79, s79, 5
	v_exp_f32_e32 v99, v99
	s_lshl_b32 s81, s63, 2
	v_exp_f32_e32 v100, v100
	s_add_i32 s81, s81, s79
	v_exp_f32_e32 v101, v101
	s_sub_i32 s78, 13, s77
	v_exp_f32_e32 v102, v102
	s_lshl_b32 s81, s81, s78
	v_exp_f32_e32 v103, v103
	s_lshr_b32 s78, 7, s77
	v_exp_f32_e32 v104, v104
	s_and_b32 s78, s76, s78
	v_exp_f32_e32 v105, v105
	s_lshl_b32 s72, s78, 10
	v_exp_f32_e32 v106, v106
	s_add_i32 s81, s81, s72
	v_exp_f32_e32 v107, v107
	s_add_i32 s72, s75, 0
	v_exp_f32_e32 v108, v108
	s_sub_i32 s80, 23, s77
	v_exp_f32_e32 v109, v109
	s_lshl_b32 s72, s72, s80
	v_exp_f32_e32 v110, v110
	s_add_i32 s81, s81, s72
	v_exp_f32_e32 v111, v111
	s_cmp_eq_u32 s77, 0
	s_cselect_b64 s[84:85], s[66:67], s[68:69]
	v_exp_f32_e32 v112, v112
	s_add_u32 s84, s84, s81
	s_addc_u32 s85, s85, 0
	v_exp_f32_e32 v113, v113
	s_lshr_b32 s80, 0x2000, s77
	v_mfma_f32_32x32x64_f8f6f4 v[66:81], v[130:137], v[122:129], 0
	v_add_f32_e64 v130, v144, v98
	v_add_f32_e64 v131, v145, v99
	v_add_f32_e64 v132, v142, v100
	v_add_f32_e64 v133, v143, v101
	v_add_f32_e64 v142, v102, v130
	v_add_f32_e64 v143, v103, v131
	v_add_f32_e64 v132, v104, v132
	v_add_f32_e64 v133, v105, v133
	v_add_f32_e64 v134, v220, v140
	v_add_f32_e64 v135, v221, v141
	v_add_f32_e64 v136, v200, v138
	v_add_f32_e64 v137, v201, v139
	s_nop 0
	s_nop 0
	s_nop 0
	s_nop 0
	s_nop 0
	s_nop 0
	v_pk_add_f32 v[142:143], v[106:107], v[142:143]
	v_pk_add_f32 v[132:133], v[108:109], v[132:133]
	v_cvt_scalef32_pk_fp8_f32 v138, v146, v147, s36
	v_cvt_scalef32_pk_fp8_f32 v139, v150, v151, s36
	v_cvt_scalef32_pk_fp8_f32 v140, v196, v197, s36
	v_cvt_scalef32_pk_fp8_f32 v141, v200, v201, s36
	v_cvt_scalef32_pk_fp8_f32 v130, v98, v99, s36
	v_cvt_scalef32_pk_fp8_f32 v131, v102, v103, s36
	v_pk_add_f32 v[146:147], v[112:113], v[132:133]
	v_pk_add_f32 v[150:151], v[110:111], v[142:143]
	v_mfma_f32_32x32x64_f8f6f4 v[50:65], v[170:177], v[184:191], v[50:65]
	v_exp_f32_e32 v82, v82
	s_and_b32 s72, s78, 3
	v_exp_f32_e32 v83, v83
	s_lshl_b32 s72, s72, 19
	v_exp_f32_e32 v84, v84
	s_lshr_b32 s81, s78, 2
; DI unsigned pk4_fp8_mul64(float a, float b, float c, float d) { v2s_t r = {0, 0}; r = __builtin_amdgcn_cvt_scalef32_pk_fp8_f32(r, a, b, 0.015625f, false); r = __builtin_amdgcn_cvt_scalef32_pk_fp8_f32(r, c, d, 0.015625f, true); return __builtin_bit_cast(unsigned, r); }
; DI f32x16 mfma8(v8i a, v8i b, f32x16 c) { return __builtin_amdgcn_mfma_scale_f32_32x32x64_f8f6f4(a, b, c, 0, 0, 0, 0, 0, 0); }
; DI void attn_unit_a8(unsigned char* lds, const AttnArgs& a) {
;     ...
;     auto w_cvt = [&]() __attribute__((always_inline)) { unsigned char* t8 = lds + AT_WT + wn4 * WPITCH + 4 * wid;
; #pragma unroll
;         for (int j = 0; j < 4; ++j) *(unsigned*)(t8 + j * WPITCH) = pk4_fp8_mul64(wq[0][j], wq[1][j], wq[2][j], wq[3][j]); };
;     const int wcol = tid >> 1, whalf = tid & 1;
;     const unsigned wper_gu = (unsigned)((wcol >> 7) * 256 + (wcol & 96) + invperm32(wcol & 31)) * 1024u + 16u * whalf;
;     const unsigned wper_dn = (unsigned)fwd_lane16(wcol) * 1024u + 16u * whalf;
;     auto w_store = [&](int j) __attribute__((always_inline)) { const float* src; unsigned char* dst; int ld, n0, k0; bool gu; w_decode(j, src, dst, ld, n0, k0, gu);
;         const int nb = n0 >> 8; const unsigned uni = (unsigned)(gu ? (nb & 3) * 512 + (nb >> 2) * 128 : nb * 256) * 1024u + (unsigned)k0;
;         const unsigned off = (gu ? wper_gu : wper_dn) + uni;
;         const unsigned* t = (const unsigned*)(lds + AT_WT + wcol * WPITCH + 16 * whalf);
;         *(u32x4*)(dst + off) = (u32x4){t[0], t[1], t[2], t[3]}; };
; DI void attn_unit_d8(unsigned char* lds, const AttnArgs& a) {
;     ...
;     auto tile = [&](const unsigned char* Kb, const unsigned char* Kn, v8i& Pa, v8i& Pb, v8i& v0, v8i& v1, const v8i& Qa, const v8i& Qb, const v8i& w0, const v8i& w1) __attribute__((always_inline)) {
;         qk(Kb, 1, s1a, s1b);
;         v0 = rd32(Kb + voff); v1 = rd32(Kb + voff + 32 * A8_PITCH);
;         o0[0] = mfma8(w0, Qa, o0[0]); o1[0] = mfma8(w0, Qb, o1[0]); o0[1] = mfma8(w1, Qa, o0[1]); o1[1] = mfma8(w1, Qb, o1[1]);
;         expsum(s0a, l0); expsum(s0b, l1); pack4(s0a, Pa, 0); pack4(s0b, Pb, 0);
;         qk(Kn, 0, s0a, s0b);
;         expsum(s1a, l0); expsum(s1b, l1); pack4(s1a, Pa, 4); pack4(s1b, Pb, 4);
; #pragma unroll
;         for (int i = 0; i < 8; ++i) { __builtin_amdgcn_sched_group_barrier(0x008, 1, 0); __builtin_amdgcn_sched_group_barrier(0x402, 22, 0); }
;     };
	v_exp_f32_e32 v85, v85
	s_lshl_b32 s81, s81, 17
	v_add_u32_e32 v102, s17, v218
	v_exp_f32_e32 v86, v86
	s_add_i32 s72, s72, s81
	v_exp_f32_e32 v87, v87
	s_lshl_b32 s81, s78, 18
	v_exp_f32_e32 v88, v88
	s_cmp_eq_u32 s77, 0
	s_cselect_b32 s72, s72, s81
	v_exp_f32_e32 v89, v89
	s_mul_i32 s81, s77, 0x10000000
	v_cvt_scalef32_pk_fp8_f32 v130, v100, v101, s36 op_sel:[0,0,0,1]
	v_cvt_scalef32_pk_fp8_f32 v131, v104, v105, s36 op_sel:[0,0,0,1]
	v_exp_f32_e32 v90, v90
	s_add_i32 s81, s81, 0x1094000
	v_exp_f32_e32 v91, v91
	s_add_i32 s72, s72, s79
	v_exp_f32_e32 v92, v92
	s_sub_i32 s73, 21, s77
	v_exp_f32_e32 v93, v93
	s_lshl_b32 s73, s75, s73
	ds_read_b128 v[98:101], v102
	ds_read_b128 v[102:105], v102 offset:16
	s_nop 0
	v_cvt_scalef32_pk_fp8_f32 v138, v148, v149, s36 op_sel:[0,0,0,1]
	v_cvt_scalef32_pk_fp8_f32 v139, v152, v153, s36 op_sel:[0,0,0,1]
	v_cvt_scalef32_pk_fp8_f32 v140, v198, v199, s36 op_sel:[0,0,0,1]
	v_cvt_scalef32_pk_fp8_f32 v141, v220, v221, s36 op_sel:[0,0,0,1]
	s_nop 0
	v_exp_f32_e32 v94, v94
	s_add_i32 s72, s72, s73
	v_mfma_f32_32x32x64_f8f6f4 v[2:17], v[170:177], v[154:161], v[2:17]
	v_exp_f32_e32 v148, v96
	s_add_u32 s72, s72, s81
	v_cvt_scalef32_pk_fp8_f32 v132, v106, v107, s36
	v_exp_f32_e32 v149, v97
	s_or_b32 s79, s72, s77
	v_pk_add_f32 v[96:97], v[136:137], v[82:83]
	v_pk_add_f32 v[106:107], v[134:135], v[84:85]
	v_exp_f32_e32 v66, v66
	v_exp_f32_e32 v67, v67
	v_exp_f32_e32 v68, v68
	v_exp_f32_e32 v69, v69
	v_exp_f32_e32 v95, v95
	v_cvt_scalef32_pk_fp8_f32 v133, v110, v111, s36
	v_pk_add_f32 v[106:107], v[88:89], v[106:107]
	v_pk_add_f32 v[96:97], v[86:87], v[96:97]
	v_exp_f32_e32 v70, v70
	v_exp_f32_e32 v71, v71
	v_exp_f32_e32 v72, v72
	v_exp_f32_e32 v73, v73
	v_cvt_scalef32_pk_fp8_f32 v132, v108, v109, s36 op_sel:[0,0,0,1]
	v_cvt_scalef32_pk_fp8_f32 v133, v112, v113, s36 op_sel:[0,0,0,1]
	v_pk_add_f32 v[96:97], v[90:91], v[96:97]
	v_pk_add_f32 v[106:107], v[92:93], v[106:107]
	v_exp_f32_e32 v74, v74
	v_mfma_f32_32x32x64_f8f6f4 v[34:49], v[162:169], v[184:191], v[34:49]
	v_exp_f32_e32 v75, v75
	v_exp_f32_e32 v76, v76
	v_exp_f32_e32 v77, v77
	v_exp_f32_e32 v78, v78
	v_exp_f32_e32 v79, v79
	s_nop 0
	v_exp_f32_e32 v80, v80
	v_exp_f32_e32 v81, v81
	s_nop 0
	s_nop 0
	v_cvt_scalef32_pk_fp8_f32 v142, v82, v83, s36
	s_nop 0
	v_cvt_scalef32_pk_fp8_f32 v143, v86, v87, s36
	v_cvt_scalef32_pk_fp8_f32 v144, v90, v91, s36
	v_cvt_scalef32_pk_fp8_f32 v142, v84, v85, s36 op_sel:[0,0,0,1]
	v_pk_add_f32 v[82:83], v[150:151], v[66:67]
	v_pk_add_f32 v[84:85], v[146:147], v[68:69]
	s_mulk_i32 s49, 0x2800
	v_pk_add_f32 v[184:185], v[148:149], v[106:107]
	v_pk_add_f32 v[186:187], v[94:95], v[96:97]
	v_cvt_scalef32_pk_fp8_f32 v145, v94, v95, s36
	v_cvt_scalef32_pk_fp8_f32 v143, v88, v89, s36 op_sel:[0,0,0,1]
	v_cvt_scalef32_pk_fp8_f32 v144, v92, v93, s36 op_sel:[0,0,0,1]
	v_mfma_f32_32x32x64_f8f6f4 v[18:33], v[162:169], v[154:161], v[18:33]
	v_add_f32_e64 v84, v72, v84
	v_add_f32_e64 v85, v73, v85
	v_add_f32_e64 v82, v70, v82
	v_add_f32_e64 v83, v71, v83
	s_nop 0
	s_nop 0
	s_nop 0
	s_nop 0
	s_add_i32 s6, s49, 0
	v_add_f32_e64 v82, v74, v82
	v_add_f32_e64 v83, v75, v83
	v_add_f32_e64 v84, v76, v84
	v_add_f32_e64 v85, v77, v85
	v_cvt_scalef32_pk_fp8_f32 v134, v66, v67, s36
	v_cvt_scalef32_pk_fp8_f32 v135, v70, v71, s36
	v_cvt_scalef32_pk_fp8_f32 v136, v74, v75, s36
	v_cvt_scalef32_pk_fp8_f32 v137, v78, v79, s36
	v_pk_add_f32 v[188:189], v[80:81], v[84:85]
	v_pk_add_f32 v[190:191], v[78:79], v[82:83]
	v_add_u32_e32 v106, s6, v216
	v_add_u32_e32 v107, s6, v217
	v_cvt_scalef32_pk_fp8_f32 v145, v148, v149, s36 op_sel:[0,0,0,1]
	v_cvt_scalef32_pk_fp8_f32 v134, v68, v69, s36 op_sel:[0,0,0,1]
	v_cvt_scalef32_pk_fp8_f32 v135, v72, v73, s36 op_sel:[0,0,0,1]
	v_cvt_scalef32_pk_fp8_f32 v136, v76, v77, s36 op_sel:[0,0,0,1]
	v_cvt_scalef32_pk_fp8_f32 v137, v80, v81, s36 op_sel:[0,0,0,1]
	s_waitcnt lgkmcnt(0)
	v_mfma_f32_32x32x64_f8f6f4 v[82:97], v[98:105], v[114:121], 0
	ds_read_b128 v[154:157], v219 offset:5120
	ds_read_b128 v[158:161], v219 offset:5136
	ds_read_b128 v[146:149], v219 offset:7680
	ds_read_b128 v[150:153], v219 offset:7696
	s_cmpk_gt_i32 s42, 0x1ff
	s_cbranch_scc1 .Lmy_rd0_ldum
	s_add_i32 s72, s61, -1
	s_cmp_lt_u32 s72, 24
	s_cbranch_scc0 .Lmy_rd0_noc
	s_waitcnt vmcnt(4)
	v_cvt_scalef32_pk_fp8_f32 v236, v236, v240, s62
	v_cvt_scalef32_pk_fp8_f32 v237, v237, v241, s62
	v_cvt_scalef32_pk_fp8_f32 v238, v238, v242, s62
	v_cvt_scalef32_pk_fp8_f32 v239, v239, v243, s62
	v_cvt_scalef32_pk_fp8_f32 v236, v244, v248, s62 op_sel:[0,0,0,1]
	v_cvt_scalef32_pk_fp8_f32 v237, v245, v249, s62 op_sel:[0,0,0,1]
	v_cvt_scalef32_pk_fp8_f32 v238, v246, v250, s62 op_sel:[0,0,0,1]
	v_cvt_scalef32_pk_fp8_f32 v239, v247, v251, s62 op_sel:[0,0,0,1]
	ds_write_b32 v252, v236
	ds_write_b32 v252, v237 offset:36
	ds_write_b32 v252, v238 offset:72
	ds_write_b32 v252, v239 offset:108

; DI unsigned pk4_fp8(float a, float b, float c, float d) { int r = 0; r = __builtin_amdgcn_cvt_pk_fp8_f32(a, b, r, false); r = __builtin_amdgcn_cvt_pk_fp8_f32(c, d, r, true); return (unsigned)r; }
; DI float clamp448(float x) { return __builtin_amdgcn_fmed3f(x, -448.0f, 448.0f); }
; DI void attn_unit_a8(unsigned char* lds, const AttnArgs& a) {
;     ...
;     float lt0 = l0[0] + l0[1] + l0[2] + l0[3];
;     lt0 += __shfl_xor(lt0, 32);
;     unsigned char* op = a.out8 + (size_t)(wid * 32 + r) * 1024 + 4 * h;
;     const float rl = 16.0f * CAT_SCALE / lt0;
; #pragma unroll
;     for (int d = 0; d < 2; ++d)
; #pragma unroll
;         for (int g = 0; g < 4; ++g) *(unsigned*)(op + 32 * d + 8 * g) = pk4_fp8(clamp448(o0[d][4 * g] * rl), clamp448(o0[d][4 * g + 1] * rl), clamp448(o0[d][4 * g + 2] * rl), clamp448(o0[d][4 * g + 3] * rl));
.LBB0_688:
	s_setprio 0
	v_add_f32_e32 v34, v108, v109
	v_add_f32_e32 v34, v110, v34
	v_add_f32_e32 v34, v111, v34
	ds_bpermute_b32 v35, v1, v34
	v_lshrrev_b32_e32 v39, 3, v153
	v_and_b32_e32 v106, 4, v39
	s_lshl_b64 s[6:7], s[22:23], 10
	s_add_u32 s4, s42, s6
	s_waitcnt lgkmcnt(0)
	v_add_f32_e32 v36, v34, v35
	v_div_scale_f32 v37, s[8:9], v36, v36, s49
	v_rcp_f32_e32 v38, v37
	s_addc_u32 s7, s43, s7
	s_add_u32 s6, s4, s57
	s_addc_u32 s7, s7, 0
	v_fma_f32 v39, -v37, v38, 1.0
	v_fmac_f32_e32 v38, v39, v38
	v_div_scale_f32 v39, vcc, s49, v36, s49
	v_mul_f32_e32 v40, v39, v38
	v_fma_f32 v41, -v37, v40, v39
	v_fmac_f32_e32 v40, v41, v38
	v_fma_f32 v37, -v37, v40, v39
	v_div_fmas_f32 v37, v37, v38, v40
	v_div_fixup_f32 v36, v37, v36, s49
	v_mul_f32_e32 v18, v18, v36
	v_mul_f32_e32 v19, v19, v36
	v_med3_f32 v18, v18, s54, v152
	v_med3_f32 v19, v19, s54, v152
	s_nop 0
	v_cvt_pk_fp8_f32 v37, v18, v19
	v_mul_f32_e32 v20, v20, v36
	v_mul_f32_e32 v19, v21, v36
	v_med3_f32 v18, v20, s54, v152
	v_med3_f32 v19, v19, s54, v152
	v_cvt_pk_fp8_f32 v37, v18, v19 op_sel:[0,0,1]
	v_mul_f32_e32 v18, v22, v36
	v_mul_f32_e32 v19, v23, v36
	v_med3_f32 v18, v18, s54, v152
	v_med3_f32 v19, v19, s54, v152
	s_nop 0
	v_cvt_pk_fp8_f32 v21, v18, v19
	v_mul_f32_e32 v20, v24, v36
	v_mul_f32_e32 v19, v25, v36
	v_med3_f32 v18, v20, s54, v152
	v_med3_f32 v19, v19, s54, v152
	v_cvt_pk_fp8_f32 v21, v18, v19 op_sel:[0,0,1]
	v_mul_f32_e32 v18, v26, v36
	v_mul_f32_e32 v19, v27, v36
	v_med3_f32 v18, v18, s54, v152
	v_med3_f32 v19, v19, s54, v152
	s_nop 0
	v_cvt_pk_fp8_f32 v22, v18, v19
	v_mul_f32_e32 v20, v28, v36
	v_mul_f32_e32 v19, v29, v36
	v_lshlrev_b64 v[34:35], 10, v[128:129]
	v_med3_f32 v18, v20, s54, v152
	v_med3_f32 v19, v19, s54, v152
	v_lshl_add_u64 v[34:35], s[6:7], 0, v[34:35]
	v_cvt_pk_fp8_f32 v22, v18, v19 op_sel:[0,0,1]
	v_lshl_add_u64 v[18:19], v[34:35], 0, v[106:107]
	global_store_dword v[18:19], v37, off
	global_store_dword v[18:19], v21, off offset:8
	global_store_dword v[18:19], v22, off offset:16
	v_mul_f32_e32 v20, v30, v36
	v_mul_f32_e32 v21, v31, v36
	v_med3_f32 v20, v20, s54, v152
	v_med3_f32 v21, v21, s54, v152
	s_nop 0
	v_cvt_pk_fp8_f32 v23, v20, v21
	v_mul_f32_e32 v22, v32, v36
	v_mul_f32_e32 v21, v33, v36
	v_med3_f32 v20, v22, s54, v152
	v_med3_f32 v21, v21, s54, v152
	v_mul_f32_e32 v2, v2, v36
	v_mul_f32_e32 v3, v3, v36
	v_cvt_pk_fp8_f32 v23, v20, v21 op_sel:[0,0,1]
	v_med3_f32 v2, v2, s54, v152
	v_med3_f32 v3, v3, s54, v152
	s_nop 0
	v_cvt_pk_fp8_f32 v20, v2, v3
	v_mul_f32_e32 v4, v4, v36
	v_mul_f32_e32 v3, v5, v36
	v_med3_f32 v2, v4, s54, v152
	v_med3_f32 v3, v3, s54, v152
	v_cvt_pk_fp8_f32 v20, v2, v3 op_sel:[0,0,1]
	v_mul_f32_e32 v2, v6, v36
	v_mul_f32_e32 v3, v7, v36
	v_med3_f32 v2, v2, s54, v152
	v_med3_f32 v3, v3, s54, v152
	s_nop 0
	v_cvt_pk_fp8_f32 v5, v2, v3
	v_mul_f32_e32 v4, v8, v36
	v_mul_f32_e32 v3, v9, v36
	v_med3_f32 v2, v4, s54, v152
	v_med3_f32 v3, v3, s54, v152
	v_cvt_pk_fp8_f32 v5, v2, v3 op_sel:[0,0,1]
	v_mul_f32_e32 v2, v10, v36
	v_mul_f32_e32 v3, v11, v36
	v_med3_f32 v2, v2, s54, v152
	v_med3_f32 v3, v3, s54, v152
	s_nop 0
	v_cvt_pk_fp8_f32 v6, v2, v3
	v_mul_f32_e32 v4, v12, v36
	v_mul_f32_e32 v3, v13, v36
	s_add_i32 s55, s55, 1
	v_med3_f32 v2, v4, s54, v152
	v_med3_f32 v3, v3, s54, v152
	s_cmp_eq_u32 s55, 2
	v_cvt_pk_fp8_f32 v6, v2, v3 op_sel:[0,0,1]
	v_mul_f32_e32 v2, v14, v36
	v_mul_f32_e32 v3, v15, v36
	s_cselect_b64 s[6:7], -1, 0
	global_store_dword v[18:19], v23, off offset:24
	global_store_dword v[18:19], v20, off offset:32
	global_store_dword v[18:19], v5, off offset:40
	global_store_dword v[18:19], v6, off offset:48
	v_med3_f32 v2, v2, s54, v152
	v_med3_f32 v3, v3, s54, v152
	s_nop 0
	s_and_b64 s[6:7], s[52:53], s[6:7]
	v_cvt_pk_fp8_f32 v5, v2, v3
	s_and_b64 s[8:9], s[26:27], s[6:7]
	s_mul_i32 s4, s55, s64
	s_and_b64 s[6:7], s[6:7], exec
	v_mul_f32_e32 v4, v16, v36
	v_mul_f32_e32 v3, v17, v36
	s_cselect_b32 s4, 0x1e0, s4
	v_med3_f32 v2, v4, s54, v152
	v_med3_f32 v3, v3, s54, v152
	s_add_i32 s4, s4, s2
	v_cvt_pk_fp8_f32 v5, v2, v3 op_sel:[0,0,1]
	s_cmpk_gt_i32 s4, 0x21f
	s_cselect_b64 s[6:7], -1, 0
	s_or_b64 s[6:7], s[8:9], s[6:7]
	s_andn2_b64 vcc, exec, s[6:7]
	global_store_dword v[18:19], v5, off offset:56
	s_cbranch_vccz .LBB0_718

; DI f32x16 mfma8(v8i a, v8i b, f32x16 c) { return __builtin_amdgcn_mfma_scale_f32_32x32x64_f8f6f4(a, b, c, 0, 0, 0, 0, 0, 0); }
; DI void attn_unit_a8(unsigned char* lds, const AttnArgs& a) {
;     ...
;     { const bf16_t* qp = a.q + (size_t)(wid * 32 + r) * 256 + 32 * h;
;       const u32x4 q0 = *(const u32x4*)qp, q1 = *(const u32x4*)(qp + 8), q2 = *(const u32x4*)(qp + 16), q3 = *(const u32x4*)(qp + 24);
;       const u32x2 c0 = bf8_to_fp8(q0), c1 = bf8_to_fp8(q1), c2 = bf8_to_fp8(q2), c3 = bf8_to_fp8(q3);
;       qf8 = (v8i){(int)c0.x, (int)c0.y, (int)c1.x, (int)c1.y, (int)c2.x, (int)c2.y, (int)c3.x, (int)c3.y}; }
;     const int lrow = tid >> 3, lch = tid & 7;
;     const unsigned char* vsrc = a.vt8 + (size_t)lrow * KEYS + 8 * lch;
;     const int ldk = lrow * A8_PITCH + 8 * lch;
;     const int ldv = A8_VOFF + lrow * A8_PITCH + (lch >> 2) * 16 + (lch & 3) * 4;
;     ...
;     if (wrider) w_issue(0);
;     gload(a.t0, kregA, vregA); gload(a.t0 + 1 < a.t1 ? a.t0 + 1 : a.t0, kregB, vregB);
;     lstore(0, kregA, vregA); lstore(1, kregB, vregB);
;     __syncthreads();
;     asm volatile("" : "+v"(qf8));
;     if (a.t0 + 2 < a.t1) gload(a.t0 + 2, kregA, vregA);
;     f32x16 sx0, sx1, sy0, sy1;
;     sx0 = mfma8(kread(lds, 0), qf8, cinit); sx1 = mfma8(kread(lds, 1), qf8, cinit);
.LBB0_700:
	s_lshl_b32 s4, s9, 5
	s_and_b32 s4, s4, 64
	s_lshl_b32 s12, s58, 7
	s_lshl_b32 s57, s9, 6
	s_ashr_i32 s11, s10, 31
	s_ashr_i32 s9, s8, 31
	s_or_b32 s12, s4, s12
	s_lshl_b64 s[10:11], s[10:11], 7
	s_lshl_b64 s[8:9], s[8:9], 7
	s_mul_hi_i32 s13, s12, 0x1100
	s_mulk_i32 s12, 0x1100
	s_add_u32 s12, s40, s12
	s_addc_u32 s13, s41, s13
	s_add_u32 s10, s38, s10
	s_addc_u32 s11, s39, s11
	s_add_u32 s58, s10, s4
	s_addc_u32 s59, s11, 0
	s_add_u32 s8, s38, s8
	s_addc_u32 s9, s39, s9
	s_add_u32 s60, s8, s4
	s_addc_u32 s61, s9, 0
	s_lshl_b32 s4, s56, 6
	v_ashrrev_i32_e32 v154, 3, v153
	v_mov_b64_e32 v[22:23], s[12:13]
	s_add_i32 s10, s4, 0xfffff000
	v_and_b32_e32 v21, 7, v153
	v_mad_i64_i32 v[22:23], s[8:9], v154, s28, v[22:23]
	s_and_b64 s[8:9], s[6:7], exec
	v_lshlrev_b32_e32 v130, 3, v21
	v_mov_b32_e32 v131, v107
	s_cselect_b32 s8, s4, s10
	v_lshl_add_u64 v[132:133], v[22:23], 0, v[130:131]
	v_add_u32_e32 v22, s8, v154
	s_cselect_b32 s9, s59, s61
	s_cselect_b32 s8, s58, s60
	s_or_b32 s12, s4, 64
	s_add_i32 s13, s4, 0xfffff040
	s_and_b64 s[10:11], s[6:7], exec
	s_cselect_b32 s10, s12, s13
	v_add_u32_e32 v28, s10, v154
	v_ashrrev_i32_e32 v23, 31, v22
	v_ashrrev_i32_e32 v29, 31, v28
	v_lshlrev_b64 v[22:23], 7, v[22:23]
	v_lshlrev_b64 v[28:29], 7, v[28:29]
	v_lshl_add_u64 v[22:23], s[8:9], 0, v[22:23]
	v_lshl_add_u64 v[28:29], s[8:9], 0, v[28:29]
	v_lshl_add_u64 v[22:23], v[22:23], 0, v[130:131]
	v_lshl_add_u64 v[24:25], v[132:133], 0, s[4:5]
	v_lshl_add_u64 v[28:29], v[28:29], 0, v[130:131]
	global_load_dwordx2 v[22:23], v[22:23], off
	s_waitcnt vmcnt(1)
	v_lshlrev_b32_e32 v32, 16, v14
	global_load_dwordx2 v[26:27], v[24:25], off
	s_nop 0
	global_load_dwordx2 v[28:29], v[28:29], off
	s_nop 0
	global_load_dwordx2 v[30:31], v[24:25], off offset:64
	v_and_b32_e32 v14, 0xffff0000, v14
	s_nop 0
	v_cvt_pk_fp8_f32 v98, v32, v14
	v_lshlrev_b32_e32 v32, 16, v16
	v_and_b32_e32 v16, 0xffff0000, v16
	s_nop 0
	v_cvt_pk_fp8_f32 v99, v32, v16
	v_lshlrev_b32_e32 v14, 16, v15
	v_and_b32_e32 v15, 0xffff0000, v15
	v_cvt_pk_fp8_f32 v98, v14, v15 op_sel:[0,0,1]
	v_lshlrev_b32_e32 v14, 16, v17
	v_and_b32_e32 v15, 0xffff0000, v17
	v_cvt_pk_fp8_f32 v99, v14, v15 op_sel:[0,0,1]
	v_lshlrev_b32_e32 v14, 16, v10
	v_and_b32_e32 v10, 0xffff0000, v10
	s_nop 0
	v_cvt_pk_fp8_f32 v100, v14, v10
	v_lshlrev_b32_e32 v14, 16, v12
	v_and_b32_e32 v12, 0xffff0000, v12
	s_nop 0
	v_cvt_pk_fp8_f32 v101, v14, v12
	v_lshlrev_b32_e32 v10, 16, v11
	v_and_b32_e32 v11, 0xffff0000, v11
	v_cvt_pk_fp8_f32 v100, v10, v11 op_sel:[0,0,1]
	v_lshlrev_b32_e32 v10, 16, v13
	v_and_b32_e32 v11, 0xffff0000, v13
	v_cvt_pk_fp8_f32 v101, v10, v11 op_sel:[0,0,1]
	v_lshlrev_b32_e32 v10, 16, v6
	v_and_b32_e32 v6, 0xffff0000, v6
	s_nop 0
	v_cvt_pk_fp8_f32 v102, v10, v6
	v_lshlrev_b32_e32 v10, 16, v8
	v_and_b32_e32 v8, 0xffff0000, v8
	s_nop 0
	v_cvt_pk_fp8_f32 v103, v10, v8
	v_lshlrev_b32_e32 v6, 16, v7
	v_and_b32_e32 v7, 0xffff0000, v7
	v_cvt_pk_fp8_f32 v102, v6, v7 op_sel:[0,0,1]
	v_lshlrev_b32_e32 v6, 16, v9
	v_and_b32_e32 v7, 0xffff0000, v9
	v_cvt_pk_fp8_f32 v103, v6, v7 op_sel:[0,0,1]
	v_lshlrev_b32_e32 v6, 16, v2
	v_and_b32_e32 v2, 0xffff0000, v2
	s_nop 0
	v_cvt_pk_fp8_f32 v104, v6, v2
	v_lshlrev_b32_e32 v6, 16, v4
	v_and_b32_e32 v4, 0xffff0000, v4
	s_nop 0
	v_cvt_pk_fp8_f32 v105, v6, v4
	v_lshlrev_b32_e32 v2, 16, v3
	v_and_b32_e32 v3, 0xffff0000, v3
	v_cvt_pk_fp8_f32 v104, v2, v3 op_sel:[0,0,1]
	v_lshlrev_b32_e32 v2, 16, v5
	v_and_b32_e32 v3, 0xffff0000, v5
	v_cvt_pk_fp8_f32 v105, v2, v3 op_sel:[0,0,1]
	v_lshlrev_b32_e32 v3, 2, v21
	v_mul_lo_u32 v2, v154, s29
	v_and_b32_e32 v4, 16, v3
	v_add_u32_e32 v155, v2, v130
	v_add_u32_e32 v2, v2, v4
	v_and_or_b32 v156, v3, 12, v2
	s_or_b32 s10, s4, 0x80
	s_addk_i32 s4, 0xf080
	v_add_u32_e32 v2, 0, v156
	s_and_b64 s[6:7], s[6:7], exec
	v_add_u32_e32 v5, 0, v155
	v_add_u32_e32 v3, 0x1400, v2
	v_add_u32_e32 v2, 0x5800, v2
	s_cselect_b32 s4, s10, s4
	s_andn2_b64 vcc, exec, s[24:25]
	s_waitcnt vmcnt(3)
	ds_write_b64 v5, v[22:23]
	s_waitcnt vmcnt(2)
	ds_write2_b32 v3, v26, v27 offset1:8
	s_waitcnt vmcnt(1)
	ds_write_b64 v5, v[28:29] offset:18048
	s_waitcnt vmcnt(0)
	ds_write2_b32 v2, v30, v31 offset0:160 offset1:168
	v_add_u32_e32 v2, s4, v154
	v_ashrrev_i32_e32 v3, 31, v2
	v_lshlrev_b64 v[2:3], 7, v[2:3]
	v_lshl_add_u64 v[2:3], s[8:9], 0, v[2:3]
	v_lshl_add_u64 v[2:3], v[2:3], 0, v[130:131]
	s_waitcnt lgkmcnt(0)
	s_barrier
	s_cmp_lt_u32 s63, 4
	s_cbranch_scc1 .Lmy_a8prio_l0
	s_setprio 1
.Lmy_a8prio_l0:
	global_load_dwordx2 v[134:135], v[2:3], off
	global_load_dwordx2 v[136:137], v[24:25], off offset:128
	v_mul_u32_u24_e32 v2, 0x50, v18
	v_add3_u32 v157, v2, v19, 0
	ds_read_b128 v[2:5], v157
	ds_read_b128 v[6:9], v157 offset:16
	s_waitcnt lgkmcnt(0)
	v_mfma_f32_32x32x64_f8f6f4 v[50:65], v[2:9], v[98:105], 0
	ds_read_b128 v[2:5], v157 offset:2560
	ds_read_b128 v[6:9], v157 offset:2576
	s_waitcnt lgkmcnt(0)
	v_mfma_f32_32x32x64_f8f6f4 v[34:49], v[2:9], v[98:105], 0
	s_cbranch_vccnz .LBB0_711
	v_ashrrev_i32_e32 v3, 1, v153
	v_lshlrev_b32_e32 v4, 2, v3
	v_and_b32_e32 v158, 16, v4
	v_lshrrev_b32_e32 v4, 1, v3
	v_and_b32_e32 v2, 0x3fff00, v153
	v_and_b32_e32 v5, 12, v4
	v_and_b32_e32 v6, 0x63, v3
	v_or3_b32 v159, v6, v2, v5
	v_lshlrev_b32_e32 v2, 4, v153
	v_and_b32_e32 v160, 16, v2
	v_lshlrev_b32_e32 v2, 4, v3
	v_lshrrev_b32_e32 v5, 2, v3
	v_and_b32_e32 v6, 0x3fff03, v3
	v_and_b32_e32 v4, 0x60, v4
	v_and_b32_e32 v5, 12, v5
	v_and_or_b32 v2, v2, s46, v6
	v_or3_b32 v161, v2, v4, v5
	v_mov_b32_e32 v2, v107
	s_lshl_b32 s16, s63, 2
	v_mad_u32_u24 v4, v20, 36, 0
	s_lshl_b32 s4, s62, 8
	v_mad_u64_u32 v[2:3], s[6:7], v3, 36, v[2:3]
	v_mov_b32_e32 v18, 0
	s_and_b32 s17, s4, 0x300
	s_and_b32 s18, s4, 0x700
	s_mov_b32 s19, 0
	v_add_u32_e32 v162, s16, v4
	v_lshlrev_b32_e32 v106, 2, v20
	v_add_u32_e32 v163, v2, v160
	s_mov_b32 s24, 0
	s_mov_b32 s14, 0
	v_mov_b32_e32 v19, v18
	v_mov_b32_e32 v20, v18
	v_mov_b32_e32 v21, v18
	v_mov_b32_e32 v22, v18
	v_mov_b32_e32 v23, v18
	v_mov_b32_e32 v24, v18
	v_mov_b32_e32 v25, v18
	v_mov_b32_e32 v26, v18
	v_mov_b32_e32 v27, v18
	v_mov_b32_e32 v28, v18
	v_mov_b32_e32 v29, v18
	v_mov_b32_e32 v30, v18
	v_mov_b32_e32 v31, v18
	v_mov_b32_e32 v32, v18
	v_mov_b32_e32 v33, v18
	v_mov_b32_e32 v2, v18
	v_mov_b32_e32 v3, v18
	v_mov_b32_e32 v4, v18
	v_mov_b32_e32 v5, v18
	v_mov_b32_e32 v6, v18
	v_mov_b32_e32 v7, v18
	v_mov_b32_e32 v8, v18
	v_mov_b32_e32 v9, v18
	v_mov_b32_e32 v10, v18
	v_mov_b32_e32 v11, v18
	v_mov_b32_e32 v12, v18
	v_mov_b32_e32 v13, v18
	v_mov_b32_e32 v14, v18
	v_mov_b32_e32 v15, v18
	v_mov_b32_e32 v16, v18
	v_mov_b32_e32 v17, v18
	v_mov_b32_e32 v108, v18
	v_mov_b32_e32 v109, v18
	v_mov_b32_e32 v110, v18
	v_mov_b32_e32 v111, v18
	s_branch .LBB0_703

; DI f32x16 mfma8(v8i a, v8i b, f32x16 c) { return __builtin_amdgcn_mfma_scale_f32_32x32x64_f8f6f4(a, b, c, 0, 0, 0, 0, 0, 0); }
; DI void attn_unit_d8(unsigned char* lds, const AttnArgs& a) {
;     ...
;     auto tile = [&](const unsigned char* Kb, const unsigned char* Kn, v8i& Pa, v8i& Pb, v8i& v0, v8i& v1, const v8i& Qa, const v8i& Qb, const v8i& w0, const v8i& w1) __attribute__((always_inline)) {
;         qk(Kb, 1, s1a, s1b);
;         v0 = rd32(Kb + voff); v1 = rd32(Kb + voff + 32 * A8_PITCH);
;         o0[0] = mfma8(w0, Qa, o0[0]); o1[0] = mfma8(w0, Qb, o1[0]); o0[1] = mfma8(w1, Qa, o0[1]); o1[1] = mfma8(w1, Qb, o1[1]);
;         expsum(s0a, l0); expsum(s0b, l1); pack4(s0a, Pa, 0); pack4(s0b, Pb, 0);
;         qk(Kn, 0, s0a, s0b);
;         expsum(s1a, l0); expsum(s1b, l1); pack4(s1a, Pa, 4); pack4(s1b, Pb, 4);
; #pragma unroll
;         for (int i = 0; i < 8; ++i) { __builtin_amdgcn_sched_group_barrier(0x008, 1, 0); __builtin_amdgcn_sched_group_barrier(0x402, 22, 0); }
;     };
;     for (int t = a.t0; t < a.t1; t += 2) {
;         const int s1 = sb + 1 >= 5 ? sb - 4 : sb + 1, s2 = sb + 2 >= 5 ? sb - 3 : sb + 2, s3 = sb + 3 >= 5 ? sb - 2 : sb + 3, s4 = sb + 4 >= 5 ? sb - 1 : sb + 4;
;         { const int ta = t + 3, tb = t + 4; gload(ta < a.t1 ? ta : a.t1 - 1, kreg0, vreg0); gload(tb < a.t1 ? tb : a.t1 - 1, kreg1, vreg1); }
;         tile(lds + sb * D8_SLOT, lds + s1 * D8_SLOT, PaX, PbX, vX0, vX1, PaY, PbY, vY0, vY1);
;         tile(lds + s1 * D8_SLOT, lds + s2 * D8_SLOT, PaY, PbY, vY0, vY1, PaX, PbX, vX0, vX1);
;         lstore(s3, kreg0, vreg0); lstore(s4, kreg1, vreg1);
;         __syncthreads();
;         sb = s2;
;     }
.LBB0_1888:
	s_add_i32 s22, s22, 2
	s_mul_i32 s8, s23, 0x2800
	s_cmp_gt_i32 s23, 3
	v_mfma_f32_32x32x64_f8f6f4 v[50:65], v[154:161], v[138:145], v[50:65]
	v_exp_f32_e32 v194, v90
	v_add_u32_e32 v90, s8, v219
	s_cselect_b32 s8, -4, 1
	s_add_i32 s51, s8, s23
	s_cmp_gt_i32 s23, 2
	s_cselect_b32 s8, -3, 2
	s_add_i32 s8, s8, s23
	s_cmp_gt_i32 s23, 1
	s_cselect_b32 s52, -2, 3
	s_add_i32 s52, s52, s23
	s_cmp_gt_i32 s23, 0
	s_cselect_b32 s53, -1, 4
	s_min_u32 s56, s22, 64
	s_add_i32 s53, s53, s23
	s_cmp_lt_u32 s22, 61
	s_mul_i32 s50, s8, 0x2800
	s_mov_b32 s23, s8
	s_cselect_b64 s[54:55], -1, 0
	s_lshl_b32 s8, s56, 6
	s_add_i32 s56, s8, 0xc0
	s_add_i32 s57, s8, 0xfffff0c0
	s_and_b64 s[54:55], s[54:55], exec
	v_lshl_add_u64 v[98:99], v[184:185], 0, s[8:9]
	s_cselect_b32 s8, s56, s57
	s_cselect_b32 s55, s19, s21
	s_cselect_b32 s54, s18, s20
	s_min_u32 s58, s22, 63
	v_exp_f32_e32 v200, v82
	v_exp_f32_e32 v201, v83
	v_exp_f32_e32 v198, v84
	v_exp_f32_e32 v199, v85
	v_exp_f32_e32 v202, v86
	v_exp_f32_e32 v203, v87
	v_exp_f32_e32 v196, v88
	v_exp_f32_e32 v197, v89
	ds_read_b128 v[82:85], v90 offset:2560
	ds_read_b128 v[86:89], v90 offset:2576
	global_load_dwordx2 v[204:205], v[98:99], off offset:192
	v_add_u32_e32 v98, s8, v182
	s_cmp_lt_u32 s22, 60
	v_ashrrev_i32_e32 v99, 31, v98
	s_cselect_b64 s[56:57], -1, 0
	s_lshl_b32 s8, s58, 6
	v_lshlrev_b64 v[98:99], 8, v[98:99]
	s_add_i32 s58, s8, 0x100
	s_add_i32 s59, s8, 0xfffff100
	v_lshl_add_u64 v[98:99], s[54:55], 0, v[98:99]
	s_and_b64 s[54:55], s[56:57], exec
	v_lshl_add_u64 v[100:101], v[184:185], 0, s[8:9]
	s_cselect_b32 s8, s58, s59
	v_lshl_add_u64 v[220:221], v[98:99], 0, v[178:179]
	v_add_u32_e32 v98, s8, v182
	v_ashrrev_i32_e32 v99, 31, v98
	s_cselect_b32 s55, s19, s21
	s_cselect_b32 s54, s18, s20
	v_lshlrev_b64 v[98:99], 8, v[98:99]
	v_lshl_add_u64 v[98:99], s[54:55], 0, v[98:99]
	global_load_dwordx2 v[206:207], v[100:101], off offset:256
	v_lshl_add_u64 v[222:223], v[98:99], 0, v[178:179]
	s_waitcnt lgkmcnt(0)
	v_mfma_f32_32x32x64_f8f6f4 v[98:113], v[82:89], v[114:121], 0
	v_exp_f32_e32 v195, v91
	v_exp_f32_e32 v224, v92
	v_exp_f32_e32 v225, v93
	v_exp_f32_e32 v226, v94
	v_exp_f32_e32 v227, v95
	v_exp_f32_e32 v228, v96
	v_exp_f32_e32 v229, v97
	ds_read_b128 v[170:173], v90 offset:5120
	ds_read_b128 v[174:177], v90 offset:5136
	ds_read_b128 v[162:165], v90 offset:7680
	ds_read_b128 v[166:169], v90 offset:7696
	v_pk_add_f32 v[90:91], v[188:189], v[200:201]
	v_pk_add_f32 v[92:93], v[186:187], v[198:199]
	v_pk_add_f32 v[90:91], v[202:203], v[90:91]
	v_pk_add_f32 v[92:93], v[196:197], v[92:93]
	v_pk_add_f32 v[90:91], v[194:195], v[90:91]
	v_pk_add_f32 v[92:93], v[224:225], v[92:93]
	v_exp_f32_e32 v66, v66
	v_exp_f32_e32 v67, v67
	v_exp_f32_e32 v68, v68
	v_exp_f32_e32 v69, v69
	v_exp_f32_e32 v70, v70
	v_exp_f32_e32 v71, v71
	v_exp_f32_e32 v72, v72
	v_pk_add_f32 v[230:231], v[228:229], v[92:93]
	v_pk_add_f32 v[232:233], v[226:227], v[90:91]
	v_mfma_f32_32x32x64_f8f6f4 v[82:97], v[82:89], v[122:129], 0
	v_exp_f32_e32 v73, v73
	v_exp_f32_e32 v74, v74
	v_exp_f32_e32 v75, v75
	v_exp_f32_e32 v76, v76
	v_exp_f32_e32 v77, v77
	v_exp_f32_e32 v78, v78
	v_exp_f32_e32 v79, v79
	v_exp_f32_e32 v80, v80
	v_exp_f32_e32 v81, v81
	v_pk_add_f32 v[188:189], v[192:193], v[66:67]
	v_pk_add_f32 v[190:191], v[190:191], v[68:69]
	s_nop 0
	v_pk_add_f32 v[188:189], v[70:71], v[188:189]
	v_pk_add_f32 v[190:191], v[72:73], v[190:191]
	s_nop 0
	v_cvt_scalef32_pk_fp8_f32 v186, v200, v201, s36
	v_pk_add_f32 v[188:189], v[74:75], v[188:189]
	v_pk_add_f32 v[190:191], v[76:77], v[190:191]
	v_cvt_scalef32_pk_fp8_f32 v187, v202, v203, s36
	v_cvt_scalef32_pk_fp8_f32 v186, v198, v199, s36 op_sel:[0,0,0,1]
	v_pk_add_f32 v[192:193], v[78:79], v[188:189]
	v_pk_add_f32 v[190:191], v[80:81], v[190:191]
	v_mfma_f32_32x32x64_f8f6f4 v[2:17], v[154:161], v[130:137], v[2:17]
	s_nop 0
	s_nop 0
	s_nop 0
	s_nop 0
	s_nop 0
	s_nop 0
	s_mulk_i32 s51, 0x2800
	v_cvt_scalef32_pk_fp8_f32 v188, v194, v195, s36
	v_cvt_scalef32_pk_fp8_f32 v189, v226, v227, s36
	v_cvt_scalef32_pk_fp8_f32 v154, v66, v67, s36
	v_cvt_scalef32_pk_fp8_f32 v155, v70, v71, s36
	v_cvt_scalef32_pk_fp8_f32 v156, v74, v75, s36
	v_cvt_scalef32_pk_fp8_f32 v157, v78, v79, s36
	v_cvt_scalef32_pk_fp8_f32 v187, v196, v197, s36 op_sel:[0,0,0,1]
	v_add_u32_e32 v234, s51, v219
	v_cvt_scalef32_pk_fp8_f32 v188, v224, v225, s36 op_sel:[0,0,0,1]
	v_cvt_scalef32_pk_fp8_f32 v189, v228, v229, s36 op_sel:[0,0,0,1]
	v_cvt_scalef32_pk_fp8_f32 v154, v68, v69, s36 op_sel:[0,0,0,1]
	v_cvt_scalef32_pk_fp8_f32 v155, v72, v73, s36 op_sel:[0,0,0,1]
	v_cvt_scalef32_pk_fp8_f32 v156, v76, v77, s36 op_sel:[0,0,0,1]
	v_cvt_scalef32_pk_fp8_f32 v157, v80, v81, s36 op_sel:[0,0,0,1]
	v_exp_f32_e32 v98, v98
	v_exp_f32_e32 v99, v99
	v_mfma_f32_32x32x64_f8f6f4 v[34:49], v[146:153], v[138:145], v[34:49]
	v_exp_f32_e32 v100, v100
	v_exp_f32_e32 v101, v101
	v_exp_f32_e32 v102, v102
	v_exp_f32_e32 v103, v103
	v_exp_f32_e32 v104, v104
	v_exp_f32_e32 v105, v105
	v_exp_f32_e32 v106, v106
	v_exp_f32_e32 v107, v107
	v_exp_f32_e32 v108, v108
	v_exp_f32_e32 v109, v109
	v_exp_f32_e32 v110, v110
	v_exp_f32_e32 v111, v111
	v_exp_f32_e32 v112, v112
	v_exp_f32_e32 v113, v113
	ds_read_b128 v[194:197], v234
	ds_read_b128 v[198:201], v234 offset:16
	v_pk_add_f32 v[66:67], v[232:233], v[98:99]
	v_pk_add_f32 v[68:69], v[230:231], v[100:101]
	v_pk_add_f32 v[66:67], v[102:103], v[66:67]
	v_pk_add_f32 v[68:69], v[104:105], v[68:69]
	v_pk_add_f32 v[66:67], v[106:107], v[66:67]
	v_pk_add_f32 v[68:69], v[108:109], v[68:69]
	v_pk_add_f32 v[140:141], v[110:111], v[66:67]
	v_pk_add_f32 v[138:139], v[112:113], v[68:69]
	v_mfma_f32_32x32x64_f8f6f4 v[18:33], v[146:153], v[130:137], v[18:33]
	v_exp_f32_e32 v82, v82
	v_exp_f32_e32 v83, v83
	v_exp_f32_e32 v84, v84
	v_exp_f32_e32 v85, v85
	v_exp_f32_e32 v86, v86
	v_exp_f32_e32 v87, v87
	v_exp_f32_e32 v88, v88
	v_exp_f32_e32 v89, v89
	v_exp_f32_e32 v90, v90
	v_exp_f32_e32 v91, v91
	v_exp_f32_e32 v92, v92
	v_exp_f32_e32 v93, v93
	v_exp_f32_e32 v94, v94
	v_exp_f32_e32 v95, v95
	v_exp_f32_e32 v96, v96
	v_exp_f32_e32 v97, v97
	v_pk_add_f32 v[66:67], v[192:193], v[82:83]
	v_pk_add_f32 v[68:69], v[190:191], v[84:85]
	v_pk_add_f32 v[66:67], v[86:87], v[66:67]
	v_pk_add_f32 v[68:69], v[88:89], v[68:69]
	v_pk_add_f32 v[130:131], v[90:91], v[66:67]
	v_pk_add_f32 v[132:133], v[92:93], v[68:69]
	s_waitcnt lgkmcnt(0)
; DI KParamsPtr kparams() { KParamsPtr p = (KParamsPtr)__builtin_amdgcn_kernarg_segment_ptr(); asm volatile("" : "+s"(p)); return p; }
; DI void attn_unit_a8(unsigned char* lds, const AttnArgs& a) {
;     ...
;     auto w_decode = [&](int j, const float*& src, unsigned char*& dst, int& ld, int& n0, int& k0, bool& gu) __attribute__((always_inline)) {
;         const int g = (j >> 2) * 512 + a.wl, e = g / 96, rr = g - e * 96; KParamsPtr kp = kparams();
;         if (rr < 64) { src = kp->w_gu + ((size_t)a.wli * NE + e) * (1024 * 2048); dst = kp->ws + WS_WGU + (size_t)a.wli * SZ_WGU + (size_t)e * 2048 * 1024; ld = 2048; n0 = (rr & 7) * 256; k0 = ((rr >> 3) * 4 + (j & 3)) * 32; gu = true; }
;         else { const int q = rr - 64; src = kp->w_dn + ((size_t)a.wli * NE + e) * (1024 * 1024); dst = kp->ws + WS_WDN + (size_t)a.wli * SZ_WDN + (size_t)e * 1024 * 1024; ld = 1024; n0 = (q & 3) * 256; k0 = ((q >> 2) * 4 + (j & 3)) * 32; gu = false; } };
;     auto w_issue = [&](int j) __attribute__((always_inline)) { const float* src; unsigned char* dst; int ld, n0, k0; bool gu; w_decode(j, src, dst, ld, n0, k0, gu);
;         const float* p = src + (size_t)(k0 + 4 * wid) * ld + n0 + wn4;
;         wq[0] = __builtin_nontemporal_load((const f32x4*)p); wq[1] = __builtin_nontemporal_load((const f32x4*)(p + ld));
;         wq[2] = __builtin_nontemporal_load((const f32x4*)(p + (size_t)2 * ld)); wq[3] = __builtin_nontemporal_load((const f32x4*)(p + (size_t)3 * ld)); };
; DI void attn_unit_d8(unsigned char* lds, const AttnArgs& a) {
;     ...
;     auto tile = [&](const unsigned char* Kb, const unsigned char* Kn, v8i& Pa, v8i& Pb, v8i& v0, v8i& v1, const v8i& Qa, const v8i& Qb, const v8i& w0, const v8i& w1) __attribute__((always_inline)) {
;         qk(Kb, 1, s1a, s1b);
;         v0 = rd32(Kb + voff); v1 = rd32(Kb + voff + 32 * A8_PITCH);
;         o0[0] = mfma8(w0, Qa, o0[0]); o1[0] = mfma8(w0, Qb, o1[0]); o0[1] = mfma8(w1, Qa, o0[1]); o1[1] = mfma8(w1, Qb, o1[1]);
;         expsum(s0a, l0); expsum(s0b, l1); pack4(s0a, Pa, 0); pack4(s0b, Pb, 0);
;         qk(Kn, 0, s0a, s0b);
;         expsum(s1a, l0); expsum(s1b, l1); pack4(s1a, Pa, 4); pack4(s1b, Pb, 4);
; #pragma unroll
;         for (int i = 0; i < 8; ++i) { __builtin_amdgcn_sched_group_barrier(0x008, 1, 0); __builtin_amdgcn_sched_group_barrier(0x402, 22, 0); }
;     };
	v_mfma_f32_32x32x64_f8f6f4 v[66:81], v[194:201], v[114:121], 0
	s_nop 0
	s_nop 0
	s_nop 0
	s_nop 0
	s_nop 0
	s_nop 0
	s_nop 0
	v_cvt_scalef32_pk_fp8_f32 v190, v98, v99, s36
	v_cvt_scalef32_pk_fp8_f32 v191, v102, v103, s36
	v_cvt_scalef32_pk_fp8_f32 v192, v106, v107, s36
	v_cvt_scalef32_pk_fp8_f32 v193, v110, v111, s36
	v_cvt_scalef32_pk_fp8_f32 v158, v82, v83, s36
	v_cvt_scalef32_pk_fp8_f32 v159, v86, v87, s36
	v_pk_add_f32 v[142:143], v[96:97], v[132:133]
	v_pk_add_f32 v[144:145], v[94:95], v[130:131]
	v_cvt_scalef32_pk_fp8_f32 v160, v90, v91, s36
	v_cvt_scalef32_pk_fp8_f32 v190, v100, v101, s36 op_sel:[0,0,0,1]
	v_cvt_scalef32_pk_fp8_f32 v191, v104, v105, s36 op_sel:[0,0,0,1]
	v_cvt_scalef32_pk_fp8_f32 v192, v108, v109, s36 op_sel:[0,0,0,1]
	v_cvt_scalef32_pk_fp8_f32 v193, v112, v113, s36 op_sel:[0,0,0,1]
	v_cvt_scalef32_pk_fp8_f32 v158, v84, v85, s36 op_sel:[0,0,0,1]
	v_cvt_scalef32_pk_fp8_f32 v159, v88, v89, s36 op_sel:[0,0,0,1]
	v_mfma_f32_32x32x64_f8f6f4 v[98:113], v[194:201], v[122:129], 0
	global_load_dwordx2 v[194:195], v[220:221], off
	global_load_dwordx2 v[196:197], v[222:223], off
	ds_read_b128 v[130:133], v234 offset:2560
	ds_read_b128 v[134:137], v234 offset:2576
	v_exp_f32_e32 v146, v66
	s_add_i32 s80, s61, 0
	v_exp_f32_e32 v147, v67
	s_lshr_b32 s73, s80, 2
	s_mulk_i32 s52, 0x2800
	s_nop 0
	s_add_i32 s8, s52, 0
	v_cvt_scalef32_pk_fp8_f32 v161, v94, v95, s36
	v_add_u32_e32 v224, s8, v183
	v_cvt_scalef32_pk_fp8_f32 v160, v92, v93, s36 op_sel:[0,0,0,1]
	v_cvt_scalef32_pk_fp8_f32 v161, v96, v97, s36 op_sel:[0,0,0,1]
	v_exp_f32_e32 v148, v68
	s_lshl_b32 s73, s73, 9
	v_exp_f32_e32 v149, v69
	s_add_i32 s73, s73, s46
	v_exp_f32_e32 v150, v70
	s_mul_i32 s75, s73, 0xaaab
	v_exp_f32_e32 v151, v71
	s_lshr_b32 s75, s75, 22
	v_exp_f32_e32 v152, v72
	s_mul_i32 s76, s75, 0x60
	v_exp_f32_e32 v153, v73
	s_sub_i32 s76, s73, s76
	v_exp_f32_e32 v198, v74
	s_lshr_b32 s77, s76, 6
	v_exp_f32_e32 v199, v75
	s_lshl_b32 s78, s77, 6
	v_exp_f32_e32 v200, v76
	s_sub_i32 s76, s76, s78
	v_exp_f32_e32 v201, v77
	s_sub_i32 s78, 3, s77
	v_exp_f32_e32 v202, v78
	s_lshr_b32 s79, s76, s78
	v_exp_f32_e32 v203, v79
	s_lshl_b32 s79, s79, 2
	v_exp_f32_e32 v220, v80
	s_and_b32 s81, s80, 3
	v_exp_f32_e32 v221, v81
	s_add_i32 s79, s79, s81
	v_pk_add_f32 v[66:67], v[140:141], v[146:147]
	s_waitcnt lgkmcnt(0)
	v_mfma_f32_32x32x64_f8f6f4 v[82:97], v[130:137], v[114:121], 0
	v_add_f32_e64 v68, v138, v148
	v_add_f32_e64 v69, v139, v149
	v_add_f32_e64 v66, v150, v66
	v_add_f32_e64 v67, v151, v67
	v_add_f32_e64 v68, v152, v68
	v_add_f32_e64 v69, v153, v69
	v_add_f32_e64 v138, v198, v66
	v_add_f32_e64 v139, v199, v67
	v_add_f32_e64 v140, v200, v68
	v_add_f32_e64 v141, v201, v69
	v_exp_f32_e32 v98, v98
	s_lshl_b32 s79, s79, 5
	v_exp_f32_e32 v99, v99
	s_lshl_b32 s81, s63, 2
	v_exp_f32_e32 v100, v100
	s_add_i32 s81, s81, s79
	v_exp_f32_e32 v101, v101
	s_sub_i32 s78, 13, s77
	v_exp_f32_e32 v102, v102
	s_lshl_b32 s81, s81, s78
	v_exp_f32_e32 v103, v103
	s_lshr_b32 s78, 7, s77
	v_exp_f32_e32 v104, v104
	s_and_b32 s78, s76, s78
	v_exp_f32_e32 v105, v105
	s_lshl_b32 s72, s78, 10
	v_exp_f32_e32 v106, v106
	s_add_i32 s81, s81, s72
	v_exp_f32_e32 v107, v107
	s_add_i32 s72, s75, 32
	v_exp_f32_e32 v108, v108
	s_sub_i32 s80, 23, s77
	v_exp_f32_e32 v109, v109
	s_lshl_b32 s72, s72, s80
	v_exp_f32_e32 v110, v110
	s_add_i32 s81, s81, s72
	v_exp_f32_e32 v111, v111
	s_cmp_eq_u32 s77, 0
	s_cselect_b64 s[84:85], s[66:67], s[68:69]
	v_exp_f32_e32 v112, v112
	s_add_u32 s84, s84, s81
	s_addc_u32 s85, s85, 0
	v_exp_f32_e32 v113, v113
	s_lshr_b32 s80, 0x2000, s77
	v_exp_f32_e32 v82, v82
	s_and_b32 s72, s78, 3
	v_mfma_f32_32x32x64_f8f6f4 v[66:81], v[130:137], v[122:129], 0
	v_add_f32_e64 v130, v144, v98
	v_add_f32_e64 v131, v145, v99
	v_add_f32_e64 v132, v142, v100
	v_add_f32_e64 v133, v143, v101
	v_add_f32_e64 v142, v102, v130
	v_add_f32_e64 v143, v103, v131
	v_add_f32_e64 v132, v104, v132
	v_add_f32_e64 v133, v105, v133
	v_add_f32_e64 v134, v220, v140
	v_add_f32_e64 v135, v221, v141
	v_add_f32_e64 v136, v202, v138
	v_add_f32_e64 v137, v203, v139
	s_nop 0
	s_nop 0
	s_nop 0
	s_nop 0
	s_nop 0
	s_nop 0
	v_pk_add_f32 v[142:143], v[106:107], v[142:143]
	v_pk_add_f32 v[132:133], v[108:109], v[132:133]
	v_cvt_scalef32_pk_fp8_f32 v138, v146, v147, s36
	v_cvt_scalef32_pk_fp8_f32 v139, v150, v151, s36
	v_cvt_scalef32_pk_fp8_f32 v140, v198, v199, s36
	v_cvt_scalef32_pk_fp8_f32 v141, v202, v203, s36
	v_cvt_scalef32_pk_fp8_f32 v130, v98, v99, s36
	v_cvt_scalef32_pk_fp8_f32 v131, v102, v103, s36
	v_pk_add_f32 v[146:147], v[112:113], v[132:133]
	v_pk_add_f32 v[150:151], v[110:111], v[142:143]
	v_mfma_f32_32x32x64_f8f6f4 v[50:65], v[170:177], v[186:193], v[50:65]
	v_exp_f32_e32 v83, v83
	s_lshl_b32 s72, s72, 19
	v_exp_f32_e32 v84, v84
	s_lshr_b32 s81, s78, 2
	v_exp_f32_e32 v85, v85
; DI unsigned pk4_fp8_mul64(float a, float b, float c, float d) { v2s_t r = {0, 0}; r = __builtin_amdgcn_cvt_scalef32_pk_fp8_f32(r, a, b, 0.015625f, false); r = __builtin_amdgcn_cvt_scalef32_pk_fp8_f32(r, c, d, 0.015625f, true); return __builtin_bit_cast(unsigned, r); }
; DI f32x16 mfma8(v8i a, v8i b, f32x16 c) { return __builtin_amdgcn_mfma_scale_f32_32x32x64_f8f6f4(a, b, c, 0, 0, 0, 0, 0, 0); }
; DI void attn_unit_a8(unsigned char* lds, const AttnArgs& a) {
;     ...
;     auto w_cvt = [&]() __attribute__((always_inline)) { unsigned char* t8 = lds + AT_WT + wn4 * WPITCH + 4 * wid;
; #pragma unroll
;         for (int j = 0; j < 4; ++j) *(unsigned*)(t8 + j * WPITCH) = pk4_fp8_mul64(wq[0][j], wq[1][j], wq[2][j], wq[3][j]); };
;     const int wcol = tid >> 1, whalf = tid & 1;
;     const unsigned wper_gu = (unsigned)((wcol >> 7) * 256 + (wcol & 96) + invperm32(wcol & 31)) * 1024u + 16u * whalf;
;     const unsigned wper_dn = (unsigned)fwd_lane16(wcol) * 1024u + 16u * whalf;
;     auto w_store = [&](int j) __attribute__((always_inline)) { const float* src; unsigned char* dst; int ld, n0, k0; bool gu; w_decode(j, src, dst, ld, n0, k0, gu);
;         const int nb = n0 >> 8; const unsigned uni = (unsigned)(gu ? (nb & 3) * 512 + (nb >> 2) * 128 : nb * 256) * 1024u + (unsigned)k0;
;         const unsigned off = (gu ? wper_gu : wper_dn) + uni;
;         const unsigned* t = (const unsigned*)(lds + AT_WT + wcol * WPITCH + 16 * whalf);
;         *(u32x4*)(dst + off) = (u32x4){t[0], t[1], t[2], t[3]}; };
; DI void attn_unit_d8(unsigned char* lds, const AttnArgs& a) {
;     ...
;     auto tile = [&](const unsigned char* Kb, const unsigned char* Kn, v8i& Pa, v8i& Pb, v8i& v0, v8i& v1, const v8i& Qa, const v8i& Qb, const v8i& w0, const v8i& w1) __attribute__((always_inline)) {
;         qk(Kb, 1, s1a, s1b);
;         v0 = rd32(Kb + voff); v1 = rd32(Kb + voff + 32 * A8_PITCH);
;         o0[0] = mfma8(w0, Qa, o0[0]); o1[0] = mfma8(w0, Qb, o1[0]); o0[1] = mfma8(w1, Qa, o0[1]); o1[1] = mfma8(w1, Qb, o1[1]);
;         expsum(s0a, l0); expsum(s0b, l1); pack4(s0a, Pa, 0); pack4(s0b, Pb, 0);
;         qk(Kn, 0, s0a, s0b);
;         expsum(s1a, l0); expsum(s1b, l1); pack4(s1a, Pa, 4); pack4(s1b, Pb, 4);
; #pragma unroll
;         for (int i = 0; i < 8; ++i) { __builtin_amdgcn_sched_group_barrier(0x008, 1, 0); __builtin_amdgcn_sched_group_barrier(0x402, 22, 0); }
;     };
	s_lshl_b32 s81, s81, 17
	v_add_u32_e32 v102, s50, v219
	v_exp_f32_e32 v86, v86
	s_add_i32 s72, s72, s81
	v_exp_f32_e32 v87, v87
	s_lshl_b32 s81, s78, 18
	v_exp_f32_e32 v88, v88
	s_cmp_eq_u32 s77, 0
	s_cselect_b32 s72, s72, s81
	v_exp_f32_e32 v89, v89
	s_mul_i32 s81, s77, 0xc000000
	v_cvt_scalef32_pk_fp8_f32 v130, v100, v101, s36 op_sel:[0,0,0,1]
	v_cvt_scalef32_pk_fp8_f32 v131, v104, v105, s36 op_sel:[0,0,0,1]
	v_exp_f32_e32 v90, v90
	s_add_i32 s81, s81, 0x9094000
	v_exp_f32_e32 v91, v91
	s_add_i32 s72, s72, s79
	v_exp_f32_e32 v92, v92
	s_sub_i32 s73, 21, s77
	v_exp_f32_e32 v93, v93
	s_lshl_b32 s73, s75, s73
	ds_read_b128 v[98:101], v102
	ds_read_b128 v[102:105], v102 offset:16
	s_nop 0
	v_cvt_scalef32_pk_fp8_f32 v138, v148, v149, s36 op_sel:[0,0,0,1]
	v_cvt_scalef32_pk_fp8_f32 v139, v152, v153, s36 op_sel:[0,0,0,1]
	v_cvt_scalef32_pk_fp8_f32 v140, v200, v201, s36 op_sel:[0,0,0,1]
	v_cvt_scalef32_pk_fp8_f32 v141, v220, v221, s36 op_sel:[0,0,0,1]
	s_nop 0
	v_exp_f32_e32 v94, v94
	s_add_i32 s72, s72, s73
	v_exp_f32_e32 v95, v95
	s_add_u32 s72, s72, s81
	v_mfma_f32_32x32x64_f8f6f4 v[2:17], v[170:177], v[154:161], v[2:17]
	v_exp_f32_e32 v148, v96
	s_or_b32 s79, s72, s77
	v_cvt_scalef32_pk_fp8_f32 v132, v106, v107, s36
	v_exp_f32_e32 v149, v97
	v_pk_add_f32 v[96:97], v[136:137], v[82:83]
	v_pk_add_f32 v[106:107], v[134:135], v[84:85]
	v_exp_f32_e32 v66, v66
	v_exp_f32_e32 v67, v67
	v_exp_f32_e32 v68, v68
	v_exp_f32_e32 v69, v69
	v_cvt_scalef32_pk_fp8_f32 v133, v110, v111, s36
	v_pk_add_f32 v[106:107], v[88:89], v[106:107]
	v_pk_add_f32 v[96:97], v[86:87], v[96:97]
	v_exp_f32_e32 v70, v70
	v_exp_f32_e32 v71, v71
	v_exp_f32_e32 v72, v72
	v_exp_f32_e32 v73, v73
	v_cvt_scalef32_pk_fp8_f32 v132, v108, v109, s36 op_sel:[0,0,0,1]
	v_cvt_scalef32_pk_fp8_f32 v133, v112, v113, s36 op_sel:[0,0,0,1]
	v_pk_add_f32 v[96:97], v[90:91], v[96:97]
	v_pk_add_f32 v[106:107], v[92:93], v[106:107]
	v_exp_f32_e32 v74, v74
	v_exp_f32_e32 v75, v75
	v_mfma_f32_32x32x64_f8f6f4 v[34:49], v[162:169], v[186:193], v[34:49]
	v_exp_f32_e32 v76, v76
	v_exp_f32_e32 v77, v77
	v_exp_f32_e32 v78, v78
	v_exp_f32_e32 v79, v79
	s_nop 0
	v_exp_f32_e32 v80, v80
	v_exp_f32_e32 v81, v81
	s_nop 0
	s_nop 0
	v_cvt_scalef32_pk_fp8_f32 v142, v82, v83, s36
	s_nop 0
	v_cvt_scalef32_pk_fp8_f32 v143, v86, v87, s36
	v_cvt_scalef32_pk_fp8_f32 v144, v90, v91, s36
	v_cvt_scalef32_pk_fp8_f32 v142, v84, v85, s36 op_sel:[0,0,0,1]
	v_pk_add_f32 v[82:83], v[150:151], v[66:67]
	v_pk_add_f32 v[84:85], v[146:147], v[68:69]
	s_mulk_i32 s53, 0x2800
	v_pk_add_f32 v[186:187], v[148:149], v[106:107]
	v_pk_add_f32 v[188:189], v[94:95], v[96:97]
	v_cvt_scalef32_pk_fp8_f32 v145, v94, v95, s36
	v_cvt_scalef32_pk_fp8_f32 v143, v88, v89, s36 op_sel:[0,0,0,1]
	v_cvt_scalef32_pk_fp8_f32 v144, v92, v93, s36 op_sel:[0,0,0,1]
	v_pk_add_f32 v[84:85], v[72:73], v[84:85]
	v_mfma_f32_32x32x64_f8f6f4 v[18:33], v[162:169], v[154:161], v[18:33]
	v_add_f32_e64 v82, v70, v82
	v_add_f32_e64 v83, v71, v83
	s_nop 0
	s_nop 0
	s_nop 0
	s_nop 0
	s_add_i32 s51, s53, 0
	v_add_f32_e64 v82, v74, v82
	v_add_f32_e64 v83, v75, v83
	v_add_f32_e64 v84, v76, v84
	v_add_f32_e64 v85, v77, v85
	v_cvt_scalef32_pk_fp8_f32 v134, v66, v67, s36
	v_cvt_scalef32_pk_fp8_f32 v135, v70, v71, s36
	v_cvt_scalef32_pk_fp8_f32 v136, v74, v75, s36
	v_cvt_scalef32_pk_fp8_f32 v137, v78, v79, s36
	v_pk_add_f32 v[190:191], v[80:81], v[84:85]
	v_pk_add_f32 v[192:193], v[78:79], v[82:83]
	v_add_u32_e32 v106, s8, v218
	v_add_u32_e32 v107, s51, v183
	v_cvt_scalef32_pk_fp8_f32 v145, v148, v149, s36 op_sel:[0,0,0,1]
	v_cvt_scalef32_pk_fp8_f32 v134, v68, v69, s36 op_sel:[0,0,0,1]
	v_cvt_scalef32_pk_fp8_f32 v135, v72, v73, s36 op_sel:[0,0,0,1]
	v_cvt_scalef32_pk_fp8_f32 v136, v76, v77, s36 op_sel:[0,0,0,1]
	v_cvt_scalef32_pk_fp8_f32 v137, v80, v81, s36 op_sel:[0,0,0,1]
	s_waitcnt lgkmcnt(0)
	v_mfma_f32_32x32x64_f8f6f4 v[82:97], v[98:105], v[114:121], 0
	ds_read_b128 v[154:157], v234 offset:5120
	ds_read_b128 v[158:161], v234 offset:5136
	ds_read_b128 v[146:149], v234 offset:7680
	ds_read_b128 v[150:153], v234 offset:7696
	s_cmpk_gt_i32 s46, 0x1ff
	s_cbranch_scc1 .Lmy_rd1_ldum
	s_add_i32 s72, s61, -1
	s_cmp_lt_u32 s72, 24
	s_cbranch_scc0 .Lmy_rd1_noc
	s_waitcnt vmcnt(4)
	v_cvt_scalef32_pk_fp8_f32 v236, v236, v240, s62
	v_cvt_scalef32_pk_fp8_f32 v237, v237, v241, s62
	v_cvt_scalef32_pk_fp8_f32 v238, v238, v242, s62
	v_cvt_scalef32_pk_fp8_f32 v239, v239, v243, s62
	v_cvt_scalef32_pk_fp8_f32 v236, v244, v248, s62 op_sel:[0,0,0,1]
	v_cvt_scalef32_pk_fp8_f32 v237, v245, v249, s62 op_sel:[0,0,0,1]
	v_cvt_scalef32_pk_fp8_f32 v238, v246, v250, s62 op_sel:[0,0,0,1]
	v_cvt_scalef32_pk_fp8_f32 v239, v247, v251, s62 op_sel:[0,0,0,1]
	ds_write_b32 v252, v236
	ds_write_b32 v252, v237 offset:36
	ds_write_b32 v252, v238 offset:72
	ds_write_b32 v252, v239 offset:108

; DI unsigned pk4_fp8(float a, float b, float c, float d) { int r = 0; r = __builtin_amdgcn_cvt_pk_fp8_f32(a, b, r, false); r = __builtin_amdgcn_cvt_pk_fp8_f32(c, d, r, true); return (unsigned)r; }
; DI float clamp448(float x) { return __builtin_amdgcn_fmed3f(x, -448.0f, 448.0f); }
; DI void attn_unit_a8(unsigned char* lds, const AttnArgs& a) {
;     ...
;     float lt0 = l0[0] + l0[1] + l0[2] + l0[3];
;     lt0 += __shfl_xor(lt0, 32);
;     unsigned char* op = a.out8 + (size_t)(wid * 32 + r) * 1024 + 4 * h;
;     const float rl = 16.0f * CAT_SCALE / lt0;
; #pragma unroll
;     for (int d = 0; d < 2; ++d)
; #pragma unroll
;         for (int g = 0; g < 4; ++g) *(unsigned*)(op + 32 * d + 8 * g) = pk4_fp8(clamp448(o0[d][4 * g] * rl), clamp448(o0[d][4 * g + 1] * rl), clamp448(o0[d][4 * g + 2] * rl), clamp448(o0[d][4 * g + 3] * rl));
.LBB0_1913:
	s_setprio 0
	v_add_f32_e32 v34, v108, v109
	v_add_f32_e32 v34, v110, v34
	v_add_f32_e32 v34, v111, v34
	ds_bpermute_b32 v35, v1, v34
	s_lshl_b64 s[10:11], s[40:41], 10
	s_add_u32 s8, s58, s10
	s_addc_u32 s11, s59, s11
	s_add_u32 s10, s8, s74
	s_addc_u32 s11, s11, 0
	s_waitcnt lgkmcnt(0)
	v_add_f32_e32 v36, v34, v35
	v_lshlrev_b64 v[34:35], 10, v[128:129]
	v_lshl_add_u64 v[34:35], s[10:11], 0, v[34:35]
	v_div_scale_f32 v37, s[10:11], v36, v36, s71
	v_rcp_f32_e32 v38, v37
	v_lshrrev_b32_e32 v39, 3, v167
	v_and_b32_e32 v106, 4, v39
	s_add_i32 s73, s73, 1
	v_fma_f32 v39, -v37, v38, 1.0
	v_fmac_f32_e32 v38, v39, v38
	v_div_scale_f32 v39, vcc, s71, v36, s71
	v_mul_f32_e32 v40, v39, v38
	v_fma_f32 v41, -v37, v40, v39
	v_fmac_f32_e32 v40, v41, v38
	v_fma_f32 v37, -v37, v40, v39
	v_div_fmas_f32 v37, v37, v38, v40
	v_div_fixup_f32 v36, v37, v36, s71
	v_mul_f32_e32 v18, v18, v36
	v_mul_f32_e32 v19, v19, v36
	v_med3_f32 v18, v18, s72, v166
	v_med3_f32 v19, v19, s72, v166
	s_nop 0
	v_cvt_pk_fp8_f32 v37, v18, v19
	v_mul_f32_e32 v20, v20, v36
	v_mul_f32_e32 v19, v21, v36
	v_med3_f32 v18, v20, s72, v166
	v_med3_f32 v19, v19, s72, v166
	v_cvt_pk_fp8_f32 v37, v18, v19 op_sel:[0,0,1]
	v_mul_f32_e32 v18, v22, v36
	v_mul_f32_e32 v19, v23, v36
	v_med3_f32 v18, v18, s72, v166
	v_med3_f32 v19, v19, s72, v166
	s_nop 0
	v_cvt_pk_fp8_f32 v21, v18, v19
	v_mul_f32_e32 v20, v24, v36
	v_mul_f32_e32 v19, v25, v36
	v_med3_f32 v18, v20, s72, v166
	v_med3_f32 v19, v19, s72, v166
	v_cvt_pk_fp8_f32 v21, v18, v19 op_sel:[0,0,1]
	v_mul_f32_e32 v18, v26, v36
	v_mul_f32_e32 v19, v27, v36
	v_med3_f32 v18, v18, s72, v166
	v_med3_f32 v19, v19, s72, v166
	s_nop 0
	v_cvt_pk_fp8_f32 v22, v18, v19
	v_mul_f32_e32 v20, v28, v36
	v_mul_f32_e32 v19, v29, v36
	v_med3_f32 v18, v20, s72, v166
	v_med3_f32 v19, v19, s72, v166
	v_cvt_pk_fp8_f32 v22, v18, v19 op_sel:[0,0,1]
	v_mul_f32_e32 v18, v30, v36
	v_mul_f32_e32 v19, v31, v36
	v_med3_f32 v18, v18, s72, v166
	v_med3_f32 v19, v19, s72, v166
	s_nop 0
	v_cvt_pk_fp8_f32 v23, v18, v19
	v_mul_f32_e32 v20, v32, v36
	v_mul_f32_e32 v19, v33, v36
	v_med3_f32 v18, v20, s72, v166
	v_med3_f32 v19, v19, s72, v166
	v_mul_f32_e32 v2, v2, v36
	v_mul_f32_e32 v3, v3, v36
	v_cvt_pk_fp8_f32 v23, v18, v19 op_sel:[0,0,1]
	v_med3_f32 v2, v2, s72, v166
	v_med3_f32 v3, v3, s72, v166
	s_nop 0
	v_cvt_pk_fp8_f32 v18, v2, v3
	v_mul_f32_e32 v4, v4, v36
	v_mul_f32_e32 v3, v5, v36
	v_med3_f32 v2, v4, s72, v166
	v_med3_f32 v3, v3, s72, v166
	v_cvt_pk_fp8_f32 v18, v2, v3 op_sel:[0,0,1]
	v_mul_f32_e32 v2, v6, v36
	v_mul_f32_e32 v3, v7, v36
	v_med3_f32 v2, v2, s72, v166
	v_med3_f32 v3, v3, s72, v166
	s_nop 0
	v_cvt_pk_fp8_f32 v5, v2, v3
	v_mul_f32_e32 v4, v8, v36
	v_mul_f32_e32 v3, v9, v36
	v_med3_f32 v2, v4, s72, v166
	v_med3_f32 v3, v3, s72, v166
	v_cvt_pk_fp8_f32 v5, v2, v3 op_sel:[0,0,1]
	v_mul_f32_e32 v2, v10, v36
	v_mul_f32_e32 v3, v11, v36
	v_med3_f32 v2, v2, s72, v166
	v_med3_f32 v3, v3, s72, v166
	s_nop 0
	v_cvt_pk_fp8_f32 v6, v2, v3
	s_cmp_eq_u32 s73, 2
	s_cselect_b64 s[10:11], -1, 0
	v_mul_f32_e32 v4, v12, v36
	v_mul_f32_e32 v3, v13, v36
	s_and_b64 s[10:11], s[46:47], s[10:11]
	v_med3_f32 v2, v4, s72, v166
	v_med3_f32 v3, v3, s72, v166
	s_and_b64 s[12:13], s[26:27], s[10:11]
	v_cvt_pk_fp8_f32 v6, v2, v3 op_sel:[0,0,1]
	v_mul_f32_e32 v2, v14, v36
	v_mul_f32_e32 v3, v15, v36
	s_mul_i32 s8, s73, s60
	s_and_b64 s[10:11], s[10:11], exec
	v_med3_f32 v2, v2, s72, v166
	v_med3_f32 v3, v3, s72, v166
	s_nop 0
	s_cselect_b32 s8, 0x1e0, s8
	v_cvt_pk_fp8_f32 v7, v2, v3
	s_add_i32 s76, s8, s2
	s_cmpk_gt_i32 s76, 0x1ff
	v_mul_f32_e32 v4, v16, v36
	v_mul_f32_e32 v3, v17, v36
	s_cselect_b64 s[10:11], -1, 0
	v_med3_f32 v2, v4, s72, v166
	v_med3_f32 v3, v3, s72, v166
	s_or_b64 s[10:11], s[12:13], s[10:11]
	v_lshl_add_u64 v[34:35], v[34:35], 0, v[106:107]
	v_cvt_pk_fp8_f32 v7, v2, v3 op_sel:[0,0,1]
	s_and_b64 vcc, exec, s[10:11]
	global_store_dword v[34:35], v37, off
	global_store_dword v[34:35], v21, off offset:8
	global_store_dword v[34:35], v22, off offset:16
	global_store_dword v[34:35], v23, off offset:24
	global_store_dword v[34:35], v18, off offset:32
	global_store_dword v[34:35], v5, off offset:40
	global_store_dword v[34:35], v6, off offset:48
	global_store_dword v[34:35], v7, off offset:56
	s_cbranch_vccnz .LBB0_1938

; DI f32x16 mfma8(v8i a, v8i b, f32x16 c) { return __builtin_amdgcn_mfma_scale_f32_32x32x64_f8f6f4(a, b, c, 0, 0, 0, 0, 0, 0); }
; DI void attn_unit_a8(unsigned char* lds, const AttnArgs& a) {
;     ...
;     { const bf16_t* qp = a.q + (size_t)(wid * 32 + r) * 256 + 32 * h;
;       const u32x4 q0 = *(const u32x4*)qp, q1 = *(const u32x4*)(qp + 8), q2 = *(const u32x4*)(qp + 16), q3 = *(const u32x4*)(qp + 24);
;       const u32x2 c0 = bf8_to_fp8(q0), c1 = bf8_to_fp8(q1), c2 = bf8_to_fp8(q2), c3 = bf8_to_fp8(q3);
;       qf8 = (v8i){(int)c0.x, (int)c0.y, (int)c1.x, (int)c1.y, (int)c2.x, (int)c2.y, (int)c3.x, (int)c3.y}; }
;     const int lrow = tid >> 3, lch = tid & 7;
;     const unsigned char* vsrc = a.vt8 + (size_t)lrow * KEYS + 8 * lch;
;     const int ldk = lrow * A8_PITCH + 8 * lch;
;     const int ldv = A8_VOFF + lrow * A8_PITCH + (lch >> 2) * 16 + (lch & 3) * 4;
;     ...
;     if (wrider) w_issue(0);
;     gload(a.t0, kregA, vregA); gload(a.t0 + 1 < a.t1 ? a.t0 + 1 : a.t0, kregB, vregB);
;     lstore(0, kregA, vregA); lstore(1, kregB, vregB);
;     __syncthreads();
;     asm volatile("" : "+v"(qf8));
;     if (a.t0 + 2 < a.t1) gload(a.t0 + 2, kregA, vregA);
;     f32x16 sx0, sx1, sy0, sy1;
;     sx0 = mfma8(kread(lds, 0), qf8, cinit); sx1 = mfma8(kread(lds, 1), qf8, cinit);
.LBB0_1920:
	s_lshl_b32 s8, s20, 5
	s_and_b32 s77, s8, 64
	s_lshl_b32 s80, s75, 7
	s_ashr_i32 s11, s10, 31
	s_or_b32 s8, s77, s80
	s_lshl_b32 s74, s20, 6
	s_lshl_b64 s[52:53], s[10:11], 7
	s_mul_hi_i32 s11, s8, 0x1100
	s_mulk_i32 s8, 0x1100
	s_add_u32 s10, s56, s8
	s_addc_u32 s11, s57, s11
	s_add_u32 s8, s54, s52
	s_addc_u32 s12, s55, s53
	v_ashrrev_i32_e32 v130, 3, v167
	v_and_b32_e32 v23, 7, v167
	v_mov_b64_e32 v[18:19], s[10:11]
	s_add_u32 s42, s8, s77
	v_ashrrev_i32_e32 v131, 31, v130
	v_mad_i64_i32 v[18:19], s[10:11], v130, s4, v[18:19]
	v_lshlrev_b32_e32 v132, 3, v23
	v_mov_b32_e32 v133, v107
	s_addc_u32 s43, s12, 0
	v_lshl_add_u64 v[134:135], v[18:19], 0, v[132:133]
	v_lshlrev_b64 v[18:19], 7, v[130:131]
	v_lshl_add_u64 v[24:25], s[42:43], 0, v[18:19]
	v_lshl_add_u64 v[24:25], v[24:25], 0, v[132:133]
	v_add_co_u32_e32 v28, vcc, s61, v24
	global_load_dwordx2 v[26:27], v[24:25], off
	s_nop 0
	v_addc_co_u32_e32 v29, vcc, 0, v25, vcc
	global_load_dwordx2 v[30:31], v[134:135], off
	s_nop 0
	global_load_dwordx2 v[28:29], v[28:29], off
	s_nop 0
	global_load_dwordx2 v[32:33], v[134:135], off offset:64
	s_waitcnt vmcnt(4)
	v_lshlrev_b32_e32 v34, 16, v14
	v_and_b32_e32 v14, 0xffff0000, v14
	s_nop 0
	v_cvt_pk_fp8_f32 v98, v34, v14
	v_lshlrev_b32_e32 v34, 16, v16
	v_and_b32_e32 v16, 0xffff0000, v16
	s_nop 0
	v_cvt_pk_fp8_f32 v99, v34, v16
	v_lshlrev_b32_e32 v14, 16, v15
	v_and_b32_e32 v15, 0xffff0000, v15
	v_cvt_pk_fp8_f32 v98, v14, v15 op_sel:[0,0,1]
	v_lshlrev_b32_e32 v14, 16, v17
	v_and_b32_e32 v15, 0xffff0000, v17
	v_cvt_pk_fp8_f32 v99, v14, v15 op_sel:[0,0,1]
	v_lshlrev_b32_e32 v14, 16, v10
	v_and_b32_e32 v10, 0xffff0000, v10
	s_nop 0
	v_cvt_pk_fp8_f32 v100, v14, v10
	v_lshlrev_b32_e32 v14, 16, v12
	v_and_b32_e32 v12, 0xffff0000, v12
	s_nop 0
	v_cvt_pk_fp8_f32 v101, v14, v12
	v_lshlrev_b32_e32 v10, 16, v11
	v_and_b32_e32 v11, 0xffff0000, v11
	v_cvt_pk_fp8_f32 v100, v10, v11 op_sel:[0,0,1]
	v_lshlrev_b32_e32 v10, 16, v13
	v_and_b32_e32 v11, 0xffff0000, v13
	v_cvt_pk_fp8_f32 v101, v10, v11 op_sel:[0,0,1]
	v_lshlrev_b32_e32 v10, 16, v6
	v_and_b32_e32 v6, 0xffff0000, v6
	s_nop 0
	v_cvt_pk_fp8_f32 v102, v10, v6
	v_lshlrev_b32_e32 v10, 16, v8
	v_and_b32_e32 v8, 0xffff0000, v8
	s_nop 0
	v_cvt_pk_fp8_f32 v103, v10, v8
	v_lshlrev_b32_e32 v6, 16, v7
	v_and_b32_e32 v7, 0xffff0000, v7
	v_cvt_pk_fp8_f32 v102, v6, v7 op_sel:[0,0,1]
	v_lshlrev_b32_e32 v6, 16, v9
	v_and_b32_e32 v7, 0xffff0000, v9
	v_cvt_pk_fp8_f32 v103, v6, v7 op_sel:[0,0,1]
	v_lshlrev_b32_e32 v6, 16, v2
	v_and_b32_e32 v2, 0xffff0000, v2
	s_nop 0
	v_cvt_pk_fp8_f32 v104, v6, v2
	v_lshlrev_b32_e32 v6, 16, v4
	v_and_b32_e32 v4, 0xffff0000, v4
	s_nop 0
	v_cvt_pk_fp8_f32 v105, v6, v4
	v_lshlrev_b32_e32 v2, 16, v3
	v_and_b32_e32 v3, 0xffff0000, v3
	v_cvt_pk_fp8_f32 v104, v2, v3 op_sel:[0,0,1]
	v_lshlrev_b32_e32 v2, 16, v5
	v_and_b32_e32 v3, 0xffff0000, v5
	v_cvt_pk_fp8_f32 v105, v2, v3 op_sel:[0,0,1]
	v_lshlrev_b32_e32 v3, 2, v23
	v_mul_lo_u32 v2, v130, s5
	v_and_b32_e32 v4, 16, v3
	v_add_u32_e32 v131, v2, v132
	v_add_u32_e32 v2, v2, v4
	v_and_or_b32 v168, v3, 12, v2
	v_add_u32_e32 v2, 0, v168
	v_add_u32_e32 v5, 0, v131
	v_add_u32_e32 v3, 0x1400, v2
	v_add_u32_e32 v2, 0x5800, v2
	s_waitcnt vmcnt(3)
	ds_write_b64 v5, v[26:27]
	s_waitcnt vmcnt(2)
	ds_write2_b32 v3, v30, v31 offset1:8
	s_waitcnt vmcnt(1)
	ds_write_b64 v5, v[28:29] offset:18048
	s_waitcnt vmcnt(0)
	ds_write2_b32 v2, v32, v33 offset0:160 offset1:168
	v_add_co_u32_e32 v2, vcc, s64, v24
	s_waitcnt lgkmcnt(0)
	s_nop 0
	v_addc_co_u32_e32 v3, vcc, 0, v25, vcc
	s_barrier
	s_cmp_lt_u32 s79, 4
	s_cbranch_scc1 .Lmy_a8prio_l1
	s_setprio 1
.Lmy_a8prio_l1:
	global_load_dwordx2 v[136:137], v[2:3], off
	global_load_dwordx2 v[138:139], v[134:135], off offset:128
	v_mul_u32_u24_e32 v2, 0x50, v21
	v_add3_u32 v169, v2, v22, 0
	ds_read_b128 v[2:5], v169
	ds_read_b128 v[6:9], v169 offset:16
	s_waitcnt lgkmcnt(0)
	v_mfma_f32_32x32x64_f8f6f4 v[34:49], v[2:9], v[98:105], 0
	ds_read_b128 v[2:5], v169 offset:2560
	ds_read_b128 v[6:9], v169 offset:2576
	s_andn2_b64 vcc, exec, s[50:51]
	s_waitcnt lgkmcnt(0)
	v_mfma_f32_32x32x64_f8f6f4 v[50:65], v[2:9], v[98:105], 0
	s_cbranch_vccnz .LBB0_1932
	v_ashrrev_i32_e32 v5, 1, v167
	v_lshlrev_b32_e32 v6, 2, v5
	v_and_b32_e32 v170, 16, v6
	v_lshrrev_b32_e32 v6, 1, v5
	v_and_b32_e32 v4, 0x3fff00, v167
	v_and_b32_e32 v7, 12, v6
	v_and_b32_e32 v8, 0x63, v5
	v_or3_b32 v171, v8, v4, v7
	v_lshlrev_b32_e32 v4, 4, v167
	v_and_b32_e32 v172, 16, v4
	v_lshlrev_b32_e32 v4, 4, v5
	v_lshrrev_b32_e32 v7, 2, v5
	v_and_b32_e32 v8, 0x3fff03, v5
	v_and_b32_e32 v6, 0x60, v6
	v_and_b32_e32 v7, 12, v7
	v_and_or_b32 v4, v4, s65, v8
	v_or3_b32 v173, v4, v6, v7
	s_lshl_b32 s20, s79, 2
	s_and_b32 s21, s78, 0x300
	s_and_b32 s22, s78, 0x700
	v_mov_b32_e32 v4, v107
	v_mad_i64_i32 v[2:3], s[10:11], v130, s4, 0
	v_mad_u64_u32 v[4:5], s[10:11], v5, 36, v[4:5]
	s_add_u32 s8, s24, s77
	s_addc_u32 s11, s25, 0
	s_add_u32 s10, s8, s52
	s_addc_u32 s11, s11, s53
	s_add_i32 s8, s80, s77
	v_lshl_add_u64 v[140:141], s[10:11], 0, v[18:19]
	s_mul_hi_i32 s11, s8, 0x1100
	s_mulk_i32 s8, 0x1100
	s_add_u32 s10, s24, s8
	v_mad_u32_u24 v6, v20, 36, 0
	s_addc_u32 s11, s25, s11
	v_mov_b32_e32 v18, 0
	v_lshl_add_u64 v[142:143], s[10:11], 0, v[2:3]
	s_mov_b32 s23, 0
	v_add_u32_e32 v174, s20, v6
	v_lshlrev_b32_e32 v106, 2, v20
	v_add_u32_e32 v175, v4, v172
	s_mov_b32 s50, 0
	s_mov_b32 s18, 0
	v_mov_b32_e32 v19, v18
	v_mov_b32_e32 v20, v18
	v_mov_b32_e32 v21, v18
	v_mov_b32_e32 v22, v18
	v_mov_b32_e32 v23, v18
	v_mov_b32_e32 v24, v18
	v_mov_b32_e32 v25, v18
	v_mov_b32_e32 v26, v18
	v_mov_b32_e32 v27, v18
	v_mov_b32_e32 v28, v18
	v_mov_b32_e32 v29, v18
	v_mov_b32_e32 v30, v18
	v_mov_b32_e32 v31, v18
	v_mov_b32_e32 v32, v18
	v_mov_b32_e32 v33, v18
	v_mov_b32_e32 v2, v18
	v_mov_b32_e32 v3, v18
	v_mov_b32_e32 v4, v18
	v_mov_b32_e32 v5, v18
	v_mov_b32_e32 v6, v18
	v_mov_b32_e32 v7, v18
	v_mov_b32_e32 v8, v18
	v_mov_b32_e32 v9, v18
	v_mov_b32_e32 v10, v18
	v_mov_b32_e32 v11, v18
	v_mov_b32_e32 v12, v18
	v_mov_b32_e32 v13, v18
	v_mov_b32_e32 v14, v18
	v_mov_b32_e32 v15, v18
	v_mov_b32_e32 v16, v18
	v_mov_b32_e32 v17, v18
	v_mov_b32_e32 v108, v18
	v_mov_b32_e32 v109, v18
	v_mov_b32_e32 v110, v18
	v_mov_b32_e32 v111, v18
	s_branch .LBB0_1923
